# xor-16/32 lane exchanges in SWA softmax and out-proj row sum-of-squares: ds_bpermute replaced by v_permlane16/32_swap on a copy (39 sites)
# speedup vs baseline: 1.0086x; 1.0025x over previous
; #define GAS __attribute__((address_space(1)))
; #define LAS __attribute__((address_space(3)))
; __device__ __forceinline__ void swa_phase(const Ctx& C, const bf16* PROJ, const float* sinks, bf16* YSWA) {
;     ...
;         for (int i = 0; i < 2; ++i) { const int task = C.tid + 512 * i, kk = 2 * (task >> 3), c8 = task & 7;
;             v4u va = {0u, 0u, 0u, 0u}, vb = {0u, 0u, 0u, 0u};
;             if (n > 0 || kk >= 128) { const bf16* vp = PROJ + (size_t)(tb - 128 + kk) * INW + C_VS + 64 * hk + 8 * c8; va = *(const GAS v4u*)vp; vb = *(const GAS v4u*)(vp + INW); }
;             LAS unsigned* dst = (LAS unsigned*)(vt + (8 * c8) * 264 + kk);
;             dst[0] = (va.x & 0xffffu) | (vb.x << 16); dst[132] = (va.x >> 16) | (vb.x & 0xffff0000u); dst[2 * 132] = (va.y & 0xffffu) | (vb.y << 16); dst[3 * 132] = (va.y >> 16) | (vb.y & 0xffff0000u);
;             dst[4 * 132] = (va.z & 0xffffu) | (vb.z << 16); dst[5 * 132] = (va.z >> 16) | (vb.z & 0xffff0000u); dst[6 * 132] = (va.w & 0xffffu) | (vb.w << 16); dst[7 * 132] = (va.w >> 16) | (vb.w & 0xffff0000u); }
;         bf16x8 kf[9][2], qf[3][2];
;         { const int q0_ = tb + 16 * w;
; #pragma unroll
;           for (int j = 0; j < 9; ++j) { const int krow = 16 * w - 128 + 16 * j + c16; int ktok = tb + krow; if (128 * n + krow < 0) ktok = b * SEQ;
;               const bf16* kp = PROJ + (size_t)ktok * INW + C_KS + 64 * hk + 8 * g4; kf[j][0] = *(const GAS bf16x8*)kp; kf[j][1] = *(const GAS bf16x8*)(kp + 32); }
; #pragma unroll
;           for (int g = 0; g < 3; ++g) { const bf16* qp = PROJ + (size_t)(q0_ + c16) * INW + C_QS + 64 * (3 * hk + g) + 8 * g4; qf[g][0] = *(const GAS bf16x8*)qp; qf[g][1] = *(const GAS bf16x8*)(qp + 32); } }
;         __syncthreads();
.LBB0_531:
	s_or_b64 exec, exec, s[26:27]
	s_waitcnt vmcnt(0)
	v_lshlrev_b32_e32 v0, 16, v4
	s_mov_b32 s22, 0xffff
	v_lshrrev_b32_e32 v1, 16, v8
	s_mov_b32 s23, 0xffff0000
	v_and_or_b32 v0, v8, s22, v0
	v_and_or_b32 v1, v4, s23, v1
	ds_write2_b32 v220, v0, v1 offset1:132
	v_lshlrev_b32_e32 v0, 16, v5
	v_lshrrev_b32_e32 v1, 16, v9
	v_and_or_b32 v0, v9, s22, v0
	v_and_or_b32 v1, v5, s23, v1
	v_add_u32_e32 v3, 0x400, v220
	ds_write2_b32 v3, v0, v1 offset0:8 offset1:140
	v_lshlrev_b32_e32 v0, 16, v6
	v_lshrrev_b32_e32 v1, 16, v10
	v_and_or_b32 v0, v10, s22, v0
	v_and_or_b32 v1, v6, s23, v1
	v_add_u32_e32 v3, 0x800, v220
	ds_write2_b32 v3, v0, v1 offset0:16 offset1:148
	v_lshlrev_b32_e32 v0, 16, v7
	v_lshrrev_b32_e32 v1, 16, v11
	v_and_or_b32 v0, v11, s22, v0
	v_and_or_b32 v1, v7, s23, v1
	v_add_u32_e32 v3, 0xc00, v220
	v_readlane_b32 s22, v255, 16
	ds_write2_b32 v3, v0, v1 offset0:24 offset1:156
	v_add_u32_e32 v0, s35, v184
	v_mov_b32_e32 v3, s21
	v_readlane_b32 s23, v255, 17
	s_lshl_b32 s30, s20, 1
	v_readlane_b32 s20, v255, 18
	v_cndmask_b32_e64 v4, v0, v3, s[22:23]
	v_readlane_b32 s22, v254, 39
	v_readlane_b32 s23, v254, 40
	v_add_u32_e32 v12, s35, v187
	v_readlane_b32 s21, v255, 19
	v_mov_b64_e32 v[0:1], s[22:23]
	s_movk_i32 s26, 0x2400
	v_cndmask_b32_e64 v12, v12, v3, s[20:21]
	v_mad_i64_i32 v[12:13], s[20:21], v12, s26, v[0:1]
	v_readlane_b32 s20, v255, 20
	v_add_u32_e32 v20, s35, v188
	v_readlane_b32 s21, v255, 21
	v_add_u32_e32 v28, s35, v189
	v_add_u32_e32 v36, s35, v190
	v_cndmask_b32_e64 v20, v20, v3, s[20:21]
	v_mad_i64_i32 v[20:21], s[20:21], v20, s26, v[0:1]
	v_readlane_b32 s20, v255, 22
	v_readlane_b32 s21, v255, 23
	v_add_u32_e32 v44, s35, v191
	v_add_u32_e32 v52, s35, v192
	v_add_u32_e32 v56, s35, v193
	v_cndmask_b32_e64 v28, v28, v3, s[20:21]
	v_cndmask_b32_e64 v36, v36, v3, s[24:25]
	v_cndmask_b32_e64 v44, v44, v3, s[0:1]
	v_cndmask_b32_e64 v52, v52, v3, s[28:29]
	v_cndmask_b32_e64 v3, v56, v3, s[16:17]
	v_mad_i64_i32 v[56:57], s[20:21], v3, s26, v[0:1]
	v_add_u32_e32 v3, s35, v183
	v_mad_i64_i32 v[4:5], s[22:23], v4, s26, v[0:1]
	v_mad_i64_i32 v[28:29], s[20:21], v28, s26, v[0:1]
	v_mad_i64_i32 v[36:37], s[20:21], v36, s26, v[0:1]
	v_mad_i64_i32 v[44:45], s[20:21], v44, s26, v[0:1]
	v_mad_i64_i32 v[52:53], s[20:21], v52, s26, v[0:1]
	v_mad_i64_i32 v[0:1], s[20:21], v3, s26, v[0:1]
	v_lshl_add_u64 v[4:5], v[4:5], 0, s[30:31]
	v_lshl_add_u64 v[12:13], v[12:13], 0, s[30:31]
	v_lshl_add_u64 v[20:21], v[20:21], 0, s[30:31]
	v_lshl_add_u64 v[28:29], v[28:29], 0, s[30:31]
	v_lshl_add_u64 v[36:37], v[36:37], 0, s[30:31]
	v_lshl_add_u64 v[44:45], v[44:45], 0, s[30:31]
	v_lshl_add_u64 v[52:53], v[52:53], 0, s[30:31]
	v_lshl_add_u64 v[56:57], v[56:57], 0, s[30:31]
	v_lshl_add_u64 v[0:1], v[0:1], 0, s[30:31]
	v_lshl_add_u64 v[8:9], v[4:5], 0, v[178:179]
	v_lshl_add_u64 v[16:17], v[12:13], 0, v[178:179]
	v_lshl_add_u64 v[24:25], v[20:21], 0, v[178:179]
	v_lshl_add_u64 v[32:33], v[28:29], 0, v[178:179]
	v_lshl_add_u64 v[40:41], v[36:37], 0, v[178:179]
	v_lshl_add_u64 v[48:49], v[44:45], 0, v[178:179]
	v_lshl_add_u64 v[52:53], v[52:53], 0, v[178:179]
	v_lshl_add_u64 v[56:57], v[56:57], 0, v[178:179]
	v_lshl_add_u64 v[0:1], v[0:1], 0, v[178:179]
	v_add_u32_e32 v3, s35, v182
	global_load_dwordx4 v[4:7], v[8:9], off offset:3584
	s_nop 0
	global_load_dwordx4 v[8:11], v[8:9], off offset:3648
	s_nop 0
	global_load_dwordx4 v[12:15], v[16:17], off offset:3584
	s_nop 0
	global_load_dwordx4 v[16:19], v[16:17], off offset:3648
	s_nop 0
	global_load_dwordx4 v[20:23], v[24:25], off offset:3584
	s_nop 0
	global_load_dwordx4 v[24:27], v[24:25], off offset:3648
	s_nop 0
	global_load_dwordx4 v[28:31], v[32:33], off offset:3584
	s_nop 0
	global_load_dwordx4 v[32:35], v[32:33], off offset:3648
	s_nop 0
	global_load_dwordx4 v[36:39], v[40:41], off offset:3584
	s_nop 0
	global_load_dwordx4 v[40:43], v[40:41], off offset:3648
	s_nop 0
	global_load_dwordx4 v[44:47], v[48:49], off offset:3584
	s_nop 0
	global_load_dwordx4 v[48:51], v[48:49], off offset:3648
	s_nop 0
	global_load_dwordx4 v[60:63], v[52:53], off offset:3584
	s_nop 0
	global_load_dwordx4 v[52:55], v[52:53], off offset:3648
	s_nop 0
	global_load_dwordx4 v[64:67], v[56:57], off offset:3584
	s_nop 0
	global_load_dwordx4 v[56:59], v[56:57], off offset:3648
	s_nop 0
	global_load_dwordx4 v[72:75], v[0:1], off offset:3584
	global_load_dwordx4 v[68:71], v[0:1], off offset:3648
	v_mad_i64_i32 v[0:1], s[22:23], v3, s26, v[176:177]
	s_mul_i32 s30, s34, 0x180
	v_lshl_add_u64 v[76:77], v[0:1], 0, s[30:31]
	global_load_dwordx4 v[88:91], v[76:77], off offset:2048
	global_load_dwordx4 v[84:87], v[76:77], off offset:2112
	s_mul_i32 s20, s34, 3
	s_lshl_b32 s21, s20, 7
	s_add_i32 s26, s21, 0x80
	s_mov_b32 s27, s31
	s_add_i32 s34, s21, 0x100
	s_mov_b32 s35, s31
	s_lshl_b32 s20, s20, 2
	v_lshl_add_u64 v[76:77], v[0:1], 0, s[26:27]
	v_lshl_add_u64 v[0:1], v[0:1], 0, s[34:35]
	s_movk_i32 s21, 0x600
	v_mov_b32_e32 v221, s20
	global_load_dwordx4 v[168:171], v[76:77], off offset:2048
	global_load_dwordx4 v[164:167], v[76:77], off offset:2112
	global_load_dwordx4 v[80:83], v[0:1], off offset:2048
	s_nop 0
	global_load_dwordx4 v[76:79], v[0:1], off offset:2112
	s_waitcnt lgkmcnt(0)
	s_barrier
; #define MFMA16(a, b, c) __builtin_amdgcn_mfma_f32_16x16x32_bf16(a, b, c, 0, 0, 0)
; __device__ __forceinline__ void swa_phase(const Ctx& C, const bf16* PROJ, const float* sinks, bf16* YSWA) {
;     ...
;         for (int g = 0; g < 3; ++g) {
;             const int h = 3 * hk + g; const float sink2 = sinks[h] * LOG2E;
;             const int q0 = tb + 16 * w;
;             f32x4 s[9];
; #pragma unroll
;             for (int j = 0; j < 9; ++j) { f32x4 a = {0.f, 0.f, 0.f, 0.f}; a = MFMA16(kf[j][0], qf[g][0], a); a = MFMA16(kf[j][1], qf[g][1], a); s[j] = a; }
;             const int qr = 16 * w + c16; float mx = -INFINITY;
; #pragma unroll
;             for (int j = 0; j < 9; ++j)
; #pragma unroll
;                 for (int r = 0; r < 4; ++r) { const int kr = 16 * w - 128 + 16 * j + 4 * g4 + r, diff = qr - kr; const bool ok = diff >= 0 && diff < 128 && (128 * n + kr) >= 0;
;                     s[j][r] = ok ? s[j][r] : -INFINITY; mx = fmaxf(mx, s[j][r]); }
;             mx = fmaxf(mx, __shfl_xor(mx, 16)); mx = fmaxf(mx, __shfl_xor(mx, 32)); mx = fmaxf(mx, sink2);
;             float sum = 0.f;
; #pragma unroll
;             for (int j = 0; j < 9; ++j)
; #pragma unroll
;                 for (int r = 0; r < 4; ++r) { const float e = __builtin_amdgcn_exp2f(s[j][r] - mx); s[j][r] = e; sum += e; }
;             sum += __shfl_xor(sum, 16); sum += __shfl_xor(sum, 32); sum += __builtin_amdgcn_exp2f(sink2 - mx);
	v_mad_i64_i32 v[180:181], s[22:23], v3, s21, v[172:173]
	global_load_dword v3, v221, s[36:37]
	s_waitcnt vmcnt(6)
	v_mfma_f32_16x16x32_bf16 v[92:95], v[4:7], v[88:91], 0
	s_mov_b32 s22, 0xff800000
	s_mov_b32 s23, 0x3fb8aa3b
	s_addk_i32 s18, 0x2000
	v_mfma_f32_16x16x32_bf16 v[96:99], v[12:15], v[88:91], 0
	s_waitcnt vmcnt(5)
	v_mfma_f32_16x16x32_bf16 v[92:95], v[8:11], v[84:87], v[92:95]
	v_mfma_f32_16x16x32_bf16 v[100:103], v[20:23], v[88:91], 0
	v_mfma_f32_16x16x32_bf16 v[104:107], v[28:31], v[88:91], 0
	s_nop 5
	v_cndmask_b32_e64 v0, v216, v92, s[40:41]
	v_cndmask_b32_e64 v1, v216, v93, s[42:43]
	v_mfma_f32_16x16x32_bf16 v[108:111], v[36:39], v[88:91], 0
	v_mfma_f32_16x16x32_bf16 v[112:115], v[44:47], v[88:91], 0
	v_mfma_f32_16x16x32_bf16 v[116:119], v[60:63], v[88:91], 0
	v_mfma_f32_16x16x32_bf16 v[120:123], v[64:67], v[88:91], 0
	v_mfma_f32_16x16x32_bf16 v[88:91], v[72:75], v[88:91], 0
	v_mfma_f32_16x16x32_bf16 v[96:99], v[16:19], v[84:87], v[96:99]
	v_mfma_f32_16x16x32_bf16 v[100:103], v[24:27], v[84:87], v[100:103]
	v_mfma_f32_16x16x32_bf16 v[104:107], v[32:35], v[84:87], v[104:107]
	s_nop 5
	v_cndmask_b32_e64 v92, v216, v97, s[50:51]
	v_cndmask_b32_e64 v93, v216, v98, s[52:53]
	v_cndmask_b32_e64 v97, v216, v102, s[60:61]
	v_mfma_f32_16x16x32_bf16 v[108:111], v[40:43], v[84:87], v[108:111]
	v_cndmask_b32_e64 v98, v216, v103, s[62:63]
	v_cndmask_b32_e64 v102, v216, v107, s[70:71]
	v_mfma_f32_16x16x32_bf16 v[112:115], v[48:51], v[84:87], v[112:115]
	v_mfma_f32_16x16x32_bf16 v[116:119], v[52:55], v[84:87], v[116:119]
	s_nop 3
	v_cndmask_b32_e64 v103, v216, v108, s[72:73]
	s_nop 1
	v_cndmask_b32_e64 v107, v216, v112, s[80:81]
	v_cndmask_b32_e64 v108, v216, v113, s[82:83]
	v_mfma_f32_16x16x32_bf16 v[120:123], v[56:59], v[84:87], v[120:123]
	v_mfma_f32_16x16x32_bf16 v[84:87], v[68:71], v[84:87], v[88:91]
	v_cndmask_b32_e64 v112, v216, v117, s[90:91]
	v_cndmask_b32_e64 v113, v216, v118, s[92:93]
	s_nop 4
	v_cndmask_b32_e64 v117, v216, v122, s[4:5]
	v_max3_f32 v88, v0, s22, v1
	v_cndmask_b32_e64 v89, v216, v94, s[44:45]
	v_cndmask_b32_e64 v90, v216, v95, s[46:47]
	v_max3_f32 v88, v88, v89, v90
	v_cndmask_b32_e64 v91, v216, v96, s[48:49]
	v_max3_f32 v88, v88, v91, v92
	v_cndmask_b32_e64 v94, v216, v99, s[54:55]
	v_max3_f32 v88, v88, v93, v94
	v_cndmask_b32_e64 v95, v216, v100, s[56:57]
	v_cndmask_b32_e64 v96, v216, v101, s[58:59]
	v_max3_f32 v88, v88, v95, v96
	v_max3_f32 v88, v88, v97, v98
	v_cndmask_b32_e64 v99, v216, v104, s[64:65]
	v_cndmask_b32_e64 v100, v216, v105, s[66:67]
	v_max3_f32 v88, v88, v99, v100
	v_cndmask_b32_e64 v101, v216, v106, s[68:69]
	v_max3_f32 v88, v88, v101, v102
	v_cndmask_b32_e64 v104, v216, v109, s[74:75]
	v_max3_f32 v88, v88, v103, v104
	v_cndmask_b32_e64 v105, v216, v110, s[76:77]
	v_cndmask_b32_e64 v106, v216, v111, s[78:79]
	v_max3_f32 v88, v88, v105, v106
	v_max3_f32 v88, v88, v107, v108
	v_cndmask_b32_e64 v109, v216, v114, s[84:85]
	v_cndmask_b32_e64 v110, v216, v115, s[86:87]
	v_max3_f32 v88, v88, v109, v110
	v_cndmask_b32_e64 v111, v216, v116, s[88:89]
	v_max3_f32 v88, v88, v111, v112
	v_cndmask_b32_e64 v114, v216, v119, s[94:95]
	v_max3_f32 v88, v88, v113, v114
	v_cndmask_b32_e64 v115, v216, v120, s[96:97]
	v_cndmask_b32_e64 v116, v216, v121, s[2:3]
	v_max3_f32 v88, v88, v115, v116
	v_cndmask_b32_e64 v118, v216, v123, s[6:7]
	v_max3_f32 v88, v88, v117, v118
	v_cndmask_b32_e64 v119, v216, v84, s[8:9]
	v_cndmask_b32_e64 v120, v216, v85, s[10:11]
	v_max3_f32 v84, v88, v119, v120
	v_cndmask_b32_e64 v121, v216, v86, s[12:13]
	v_cndmask_b32_e64 v122, v216, v87, s[14:15]
	v_max3_f32 v84, v84, v121, v122
	v_mov_b32_e32 v86, v84
	s_nop 1
	v_permlane16_swap_b32_e32 v86, v84
	s_waitcnt vmcnt(0)
	v_mul_f32_e32 v85, 0x3fb8aa3b, v3
	v_mfma_f32_16x16x32_bf16 v[242:245], v[44:47], v[168:171], 0
	s_waitcnt lgkmcnt(0)
	v_max_f32_e32 v86, v86, v86
	v_max_f32_e32 v84, v84, v86
	v_mov_b32_e32 v86, v84
	s_nop 1
	v_permlane32_swap_b32_e32 v86, v84
	v_mfma_f32_16x16x32_bf16 v[246:249], v[60:63], v[168:171], 0
	s_waitcnt lgkmcnt(0)
	v_max3_f32 v123, v84, v86, v85
	v_sub_f32_e32 v88, v93, v123
	v_sub_f32_e32 v93, v98, v123
	v_sub_f32_e32 v98, v103, v123
	v_sub_f32_e32 v103, v108, v123
	v_sub_f32_e32 v108, v113, v123
	v_sub_f32_e32 v87, v92, v123
	v_sub_f32_e32 v92, v97, v123
	v_sub_f32_e32 v97, v102, v123
	v_sub_f32_e32 v102, v107, v123
	v_sub_f32_e32 v107, v112, v123
	v_exp_f32_e32 v112, v108
	v_sub_f32_e32 v108, v114, v123
	v_exp_f32_e32 v113, v108
	v_sub_f32_e32 v108, v115, v123
	v_exp_f32_e32 v114, v108
	v_sub_f32_e32 v108, v116, v123
	v_exp_f32_e32 v115, v108
	v_sub_f32_e32 v108, v117, v123
	v_sub_f32_e32 v0, v0, v123
	v_exp_f32_e32 v116, v108
	v_sub_f32_e32 v108, v118, v123
	v_exp_f32_e32 v0, v0
	v_sub_f32_e32 v1, v1, v123
	v_exp_f32_e32 v117, v108
	v_sub_f32_e32 v108, v119, v123
	v_exp_f32_e32 v1, v1
	v_sub_f32_e32 v84, v89, v123
	v_exp_f32_e32 v118, v108
	v_sub_f32_e32 v108, v120, v123
	v_exp_f32_e32 v84, v84
	v_sub_f32_e32 v85, v90, v123
	v_exp_f32_e32 v119, v108
	v_sub_f32_e32 v108, v121, v123
	v_exp_f32_e32 v85, v85
	v_sub_f32_e32 v86, v91, v123
	v_exp_f32_e32 v120, v108
	v_sub_f32_e32 v108, v122, v123
	v_exp_f32_e32 v86, v86
	v_exp_f32_e32 v121, v108
	v_add_f32_e32 v108, 0, v0
	v_exp_f32_e32 v87, v87
	v_add_f32_e32 v108, v1, v108
	v_exp_f32_e32 v88, v88
	v_sub_f32_e32 v89, v94, v123
	v_add_f32_e32 v108, v84, v108
	v_exp_f32_e32 v89, v89
	v_sub_f32_e32 v90, v95, v123
	v_add_f32_e32 v108, v85, v108
	v_exp_f32_e32 v90, v90
	v_sub_f32_e32 v91, v96, v123
	v_add_f32_e32 v108, v86, v108
	v_exp_f32_e32 v91, v91
	v_add_f32_e32 v108, v87, v108
	v_exp_f32_e32 v92, v92
	v_add_f32_e32 v108, v88, v108
	v_exp_f32_e32 v93, v93
; #define LAS __attribute__((address_space(3)))
; __device__ __forceinline__ unsigned pk2(float lo, float hi) { f32x2_m v = {lo, hi}; bf16x2_m b = __builtin_convertvector(v, bf16x2_m); return __builtin_bit_cast(unsigned, b); }
; #define MFMA16(a, b, c) __builtin_amdgcn_mfma_f32_16x16x32_bf16(a, b, c, 0, 0, 0)
; __device__ __forceinline__ void swa_phase(const Ctx& C, const bf16* PROJ, const float* sinks, bf16* YSWA) {
;     ...
;             float sum = 0.f;
; #pragma unroll
;             for (int j = 0; j < 9; ++j)
; #pragma unroll
;                 for (int r = 0; r < 4; ++r) { const float e = __builtin_amdgcn_exp2f(s[j][r] - mx); s[j][r] = e; sum += e; }
;             sum += __shfl_xor(sum, 16); sum += __shfl_xor(sum, 32); sum += __builtin_amdgcn_exp2f(sink2 - mx);
;             const float inv = 1.0f / sum;
;             unsigned pw[10][2];
; #pragma unroll
;             for (int j = 0; j < 9; ++j) { pw[j][0] = pk2(s[j][0] * inv, s[j][1] * inv); pw[j][1] = pk2(s[j][2] * inv, s[j][3] * inv); }
;             pw[9][0] = 0u; pw[9][1] = 0u;
;             f32x4 o[4];
; #pragma unroll
;             for (int dt = 0; dt < 4; ++dt) o[dt] = (f32x4){0.f, 0.f, 0.f, 0.f};
; #pragma unroll
;             for (int sI = 0; sI < 5; ++sI) {
;                 const v4u pb = {pw[2 * sI][0], pw[2 * sI][1], pw[2 * sI + 1][0], pw[2 * sI + 1][1]};
;                 const int kkA = 16 * w + 32 * sI + 4 * g4; int kkB = kkA + 16; if (kkB > 252) kkB = 252;
; #pragma unroll
;                 for (int dt = 0; dt < 4; ++dt) { const LAS bf16* vp = vt + (16 * dt + c16) * 264;
;                     const v2u va = *(const LAS v2u*)(vp + kkA), vb = *(const LAS v2u*)(vp + kkB);
;                     const v4u av = {va.x, va.y, vb.x, vb.y};
;                     o[dt] = MFMA16(__builtin_bit_cast(bf16x8, av), __builtin_bit_cast(bf16x8, pb), o[dt]); }
	v_sub_f32_e32 v94, v99, v123
	v_add_f32_e32 v108, v89, v108
	v_exp_f32_e32 v94, v94
	v_sub_f32_e32 v95, v100, v123
	v_add_f32_e32 v108, v90, v108
	v_exp_f32_e32 v95, v95
	v_sub_f32_e32 v96, v101, v123
	v_add_f32_e32 v108, v91, v108
	v_exp_f32_e32 v96, v96
	v_add_f32_e32 v108, v92, v108
	v_exp_f32_e32 v97, v97
	v_add_f32_e32 v108, v93, v108
	v_exp_f32_e32 v98, v98
	v_sub_f32_e32 v99, v104, v123
	v_add_f32_e32 v108, v94, v108
	v_exp_f32_e32 v99, v99
	v_sub_f32_e32 v100, v105, v123
	v_add_f32_e32 v108, v95, v108
	v_exp_f32_e32 v100, v100
	v_sub_f32_e32 v101, v106, v123
	v_add_f32_e32 v108, v96, v108
	v_exp_f32_e32 v101, v101
	v_add_f32_e32 v108, v97, v108
	v_exp_f32_e32 v102, v102
	v_add_f32_e32 v108, v98, v108
	v_exp_f32_e32 v103, v103
	v_sub_f32_e32 v104, v109, v123
	v_add_f32_e32 v108, v99, v108
	v_exp_f32_e32 v104, v104
	v_sub_f32_e32 v105, v110, v123
	v_add_f32_e32 v108, v100, v108
	v_exp_f32_e32 v105, v105
	v_sub_f32_e32 v106, v111, v123
	v_add_f32_e32 v108, v101, v108
	v_exp_f32_e32 v106, v106
	v_add_f32_e32 v108, v102, v108
	v_exp_f32_e32 v107, v107
	v_add_f32_e32 v108, v103, v108
	v_add_f32_e32 v108, v104, v108
	v_add_f32_e32 v108, v105, v108
	v_add_f32_e32 v108, v106, v108
	v_add_f32_e32 v108, v107, v108
	v_add_f32_e32 v108, v112, v108
	v_add_f32_e32 v108, v113, v108
	v_add_f32_e32 v108, v114, v108
	v_add_f32_e32 v108, v115, v108
	v_add_f32_e32 v108, v116, v108
	v_add_f32_e32 v108, v117, v108
	v_add_f32_e32 v108, v118, v108
	v_add_f32_e32 v108, v119, v108
	v_add_f32_e32 v108, v120, v108
	v_add_f32_e32 v108, v121, v108
	v_mov_b32_e32 v109, v108
	s_nop 1
	v_permlane16_swap_b32_e32 v109, v108
	v_fma_f32 v3, v3, s23, -v123
	v_exp_f32_e32 v3, v3
	v_mfma_f32_16x16x32_bf16 v[242:245], v[48:51], v[164:167], v[242:245]
	s_waitcnt lgkmcnt(0)
	v_add_f32_e32 v108, v108, v109
	v_mov_b32_e32 v109, v108
	s_nop 1
	v_permlane32_swap_b32_e32 v109, v108
	v_mfma_f32_16x16x32_bf16 v[246:249], v[52:55], v[164:167], v[246:249]
	s_waitcnt lgkmcnt(0)
	v_add_f32_e32 v108, v108, v109
	v_add_f32_e32 v3, v3, v108
	v_div_scale_f32 v108, s[20:21], v3, v3, 1.0
	v_rcp_f32_e32 v109, v108
	s_nop 0
	v_fma_f32 v110, -v108, v109, 1.0
	v_fmac_f32_e32 v109, v110, v109
	v_div_scale_f32 v110, vcc, 1.0, v3, 1.0
	v_mul_f32_e32 v111, v110, v109
	v_fma_f32 v122, -v108, v111, v110
	v_fmac_f32_e32 v111, v122, v109
	v_fma_f32 v108, -v108, v111, v110
	v_div_fmas_f32 v108, v108, v109, v111
	v_div_fixup_f32 v122, v108, v3, 1.0
	v_pk_mul_f32 v[0:1], v[0:1], v[122:123] op_sel_hi:[1,0]
	v_add_u32_e32 v3, 0x100, v194
	v_cvt_pk_bf16_f32 v108, v0, v1
	v_pk_mul_f32 v[0:1], v[84:85], v[122:123] op_sel_hi:[1,0]
	v_pk_mul_f32 v[84:85], v[120:121], v[122:123] op_sel_hi:[1,0]
	v_cvt_pk_bf16_f32 v109, v0, v1
	v_pk_mul_f32 v[0:1], v[86:87], v[122:123] op_sel_hi:[1,0]
	s_nop 0
	v_cvt_pk_bf16_f32 v110, v0, v1
	v_pk_mul_f32 v[0:1], v[88:89], v[122:123] op_sel_hi:[1,0]
	s_nop 0
	v_cvt_pk_bf16_f32 v111, v0, v1
	v_pk_mul_f32 v[0:1], v[90:91], v[122:123] op_sel_hi:[1,0]
	s_nop 0
	v_cvt_pk_bf16_f32 v124, v0, v1
	v_pk_mul_f32 v[0:1], v[92:93], v[122:123] op_sel_hi:[1,0]
	s_nop 0
	v_cvt_pk_bf16_f32 v125, v0, v1
	v_pk_mul_f32 v[0:1], v[94:95], v[122:123] op_sel_hi:[1,0]
	s_nop 0
	v_cvt_pk_bf16_f32 v126, v0, v1
	v_pk_mul_f32 v[0:1], v[96:97], v[122:123] op_sel_hi:[1,0]
	s_nop 0
	v_cvt_pk_bf16_f32 v127, v0, v1
	v_pk_mul_f32 v[0:1], v[98:99], v[122:123] op_sel_hi:[1,0]
	s_nop 0
	v_cvt_pk_bf16_f32 v140, v0, v1
	v_pk_mul_f32 v[0:1], v[100:101], v[122:123] op_sel_hi:[1,0]
	s_nop 0
	v_cvt_pk_bf16_f32 v141, v0, v1
	v_pk_mul_f32 v[0:1], v[102:103], v[122:123] op_sel_hi:[1,0]
	s_nop 0
	v_cvt_pk_bf16_f32 v142, v0, v1
	v_pk_mul_f32 v[0:1], v[104:105], v[122:123] op_sel_hi:[1,0]
	s_nop 0
	v_cvt_pk_bf16_f32 v143, v0, v1
	v_pk_mul_f32 v[0:1], v[106:107], v[122:123] op_sel_hi:[1,0]
	s_nop 0
	v_cvt_pk_bf16_f32 v156, v0, v1
	v_pk_mul_f32 v[0:1], v[112:113], v[122:123] op_sel_hi:[1,0]
	s_nop 0
	v_cvt_pk_bf16_f32 v157, v0, v1
	v_pk_mul_f32 v[0:1], v[114:115], v[122:123] op_sel_hi:[1,0]
	ds_read2_b64 v[112:115], v194 offset1:8
	ds_read_b64 v[94:95], v195 offset:32
	v_cvt_pk_bf16_f32 v158, v0, v1
	v_pk_mul_f32 v[0:1], v[116:117], v[122:123] op_sel_hi:[1,0]
	s_waitcnt lgkmcnt(1)
	v_mov_b32_e32 v92, v112
	v_cvt_pk_bf16_f32 v159, v0, v1
	v_pk_mul_f32 v[0:1], v[118:119], v[122:123] op_sel_hi:[1,0]
	v_mov_b32_e32 v93, v113
	v_cvt_pk_bf16_f32 v0, v0, v1
	v_cvt_pk_bf16_f32 v1, v84, v85
	ds_read2st64_b64 v[84:87], v3 offset1:16
	ds_read_b64 v[98:99], v195 offset:8480
	s_waitcnt lgkmcnt(2)
	v_mfma_f32_16x16x32_bf16 v[116:119], v[92:95], v[108:111], 0
	s_waitcnt lgkmcnt(1)
	v_mov_b32_e32 v96, v86
	v_add_u32_e32 v86, 0x4000, v194
	ds_read2_b64 v[128:131], v86 offset0:64 offset1:72
	ds_read_b64 v[102:103], v195 offset:16928
	ds_read2st64_b64 v[88:91], v3 offset0:33 offset1:49
	ds_read_b64 v[106:107], v195 offset:25376
	v_mov_b32_e32 v97, v87
	v_add_u32_e32 v3, 0x2000, v194
	s_waitcnt lgkmcnt(3)
	v_mov_b32_e32 v100, v128
	v_mov_b32_e32 v101, v129
	s_waitcnt lgkmcnt(1)
	v_mov_b32_e32 v104, v90
	v_mov_b32_e32 v105, v91
	v_mfma_f32_16x16x32_bf16 v[120:123], v[96:99], v[108:111], 0
	v_add_u32_e32 v87, 0x6000, v194
	v_mfma_f32_16x16x32_bf16 v[132:135], v[100:103], v[108:111], 0
	s_waitcnt lgkmcnt(0)
	v_mfma_f32_16x16x32_bf16 v[136:139], v[104:107], v[108:111], 0
	ds_read_b64 v[110:111], v196 offset:32
	v_mov_b32_e32 v108, v114
	v_mov_b32_e32 v109, v115
	ds_read2_b64 v[148:151], v3 offset0:40 offset1:48
	ds_read_b64 v[114:115], v196 offset:8480
	s_waitcnt lgkmcnt(2)
	v_mfma_f32_16x16x32_bf16 v[144:147], v[108:111], v[124:127], v[116:119]
	s_waitcnt lgkmcnt(1)
	v_mov_b32_e32 v112, v148
	v_mov_b32_e32 v113, v149
	ds_read_b64 v[118:119], v196 offset:16928
	v_mov_b32_e32 v116, v130
	s_waitcnt lgkmcnt(1)
; #define LAS __attribute__((address_space(3)))
; __device__ __forceinline__ void swa_phase(const Ctx& C, const bf16* PROJ, const float* sinks, bf16* YSWA) {
;     ...
;             for (int j = 0; j < 9; ++j) { f32x4 a = {0.f, 0.f, 0.f, 0.f}; a = MFMA16(kf[j][0], qf[g][0], a); a = MFMA16(kf[j][1], qf[g][1], a); s[j] = a; }
;             const int qr = 16 * w + c16; float mx = -INFINITY;
; #pragma unroll
;             for (int j = 0; j < 9; ++j)
; #pragma unroll
;                 for (int r = 0; r < 4; ++r) { const int kr = 16 * w - 128 + 16 * j + 4 * g4 + r, diff = qr - kr; const bool ok = diff >= 0 && diff < 128 && (128 * n + kr) >= 0;
;                     s[j][r] = ok ? s[j][r] : -INFINITY; mx = fmaxf(mx, s[j][r]); }
;             mx = fmaxf(mx, __shfl_xor(mx, 16)); mx = fmaxf(mx, __shfl_xor(mx, 32)); mx = fmaxf(mx, sink2);
;             float sum = 0.f;
; #pragma unroll
;             for (int j = 0; j < 9; ++j)
; #pragma unroll
;                 for (int r = 0; r < 4; ++r) { const float e = __builtin_amdgcn_exp2f(s[j][r] - mx); s[j][r] = e; sum += e; }
;             sum += __shfl_xor(sum, 16); sum += __shfl_xor(sum, 32); sum += __builtin_amdgcn_exp2f(sink2 - mx);
;             const float inv = 1.0f / sum;
;             unsigned pw[10][2];
; #pragma unroll
;             for (int j = 0; j < 9; ++j) { pw[j][0] = pk2(s[j][0] * inv, s[j][1] * inv); pw[j][1] = pk2(s[j][2] * inv, s[j][3] * inv); }
;             pw[9][0] = 0u; pw[9][1] = 0u;
;             f32x4 o[4];
; #pragma unroll
;             for (int dt = 0; dt < 4; ++dt) o[dt] = (f32x4){0.f, 0.f, 0.f, 0.f};
; #pragma unroll
;             for (int sI = 0; sI < 5; ++sI) {
;                 const v4u pb = {pw[2 * sI][0], pw[2 * sI][1], pw[2 * sI + 1][0], pw[2 * sI + 1][1]};
;                 const int kkA = 16 * w + 32 * sI + 4 * g4; int kkB = kkA + 16; if (kkB > 252) kkB = 252;
; #pragma unroll
;                 for (int dt = 0; dt < 4; ++dt) { const LAS bf16* vp = vt + (16 * dt + c16) * 264;
;                     const v2u va = *(const LAS v2u*)(vp + kkA), vb = *(const LAS v2u*)(vp + kkB);
;                     const v4u av = {va.x, va.y, vb.x, vb.y};
;                     o[dt] = MFMA16(__builtin_bit_cast(bf16x8, av), __builtin_bit_cast(bf16x8, pb), o[dt]); }
;             }
;             bf16* op = YSWA + (size_t)(q0 + c16) * 768 + 64 * h + 4 * g4;
; #pragma unroll
	v_mfma_f32_16x16x32_bf16 v[152:155], v[112:115], v[124:127], v[120:123]
	ds_read2_b64 v[222:225], v87 offset0:104 offset1:112
	s_nop 1
	ds_read_b64 v[122:123], v196 offset:25376
	v_mov_b32_e32 v117, v131
	v_mov_b32_e32 v128, v150
	v_mov_b32_e32 v129, v151
	s_waitcnt lgkmcnt(1)
	v_mov_b32_e32 v120, v222
	v_mov_b32_e32 v121, v223
	v_mfma_f32_16x16x32_bf16 v[160:163], v[116:119], v[124:127], v[132:135]
	s_waitcnt lgkmcnt(0)
	v_mfma_f32_16x16x32_bf16 v[226:229], v[120:123], v[124:127], v[136:139]
	ds_read2_b64 v[230:233], v194 offset0:16 offset1:24
	ds_read_b64 v[126:127], v197 offset:32
	ds_read_b64 v[130:131], v197 offset:8480
	v_mov_b32_e32 v136, v224
	s_waitcnt lgkmcnt(0)
	v_mfma_f32_16x16x32_bf16 v[148:151], v[128:131], v[140:143], v[152:155]
	s_nop 2
	ds_read2_b64 v[152:155], v86 offset0:80 offset1:88
	ds_read_b64 v[134:135], v197 offset:16928
	ds_read_b64 v[138:139], v197 offset:25376
	v_mov_b32_e32 v124, v230
	v_mov_b32_e32 v125, v231
	s_waitcnt lgkmcnt(2)
	v_mov_b32_e32 v132, v152
	v_mov_b32_e32 v133, v153
	v_mov_b32_e32 v137, v225
	v_mfma_f32_16x16x32_bf16 v[144:147], v[124:127], v[140:143], v[144:147]
	s_waitcnt lgkmcnt(1)
	v_mfma_f32_16x16x32_bf16 v[160:163], v[132:135], v[140:143], v[160:163]
	s_waitcnt lgkmcnt(0)
	v_mfma_f32_16x16x32_bf16 v[222:225], v[136:139], v[140:143], v[226:229]
	ds_read_b64 v[142:143], v204 offset:32
	v_mov_b32_e32 v140, v232
	v_mov_b32_e32 v141, v233
	s_waitcnt lgkmcnt(0)
	s_nop 0
	v_mfma_f32_16x16x32_bf16 v[226:229], v[140:143], v[156:159], v[144:147]
	ds_read2_b64 v[230:233], v3 offset0:56 offset1:64
	s_nop 1
	ds_read_b64 v[146:147], v204 offset:8480
	v_mov_b32_e32 v3, v2
	s_waitcnt lgkmcnt(1)
	v_mov_b32_e32 v144, v230
	v_mov_b32_e32 v145, v231
	s_waitcnt lgkmcnt(0)
	s_nop 0
	v_mfma_f32_16x16x32_bf16 v[234:237], v[144:147], v[156:159], v[148:151]
	s_nop 2
	ds_read_b64 v[150:151], v204 offset:16928
	v_mov_b32_e32 v148, v154
	v_mov_b32_e32 v149, v155
	ds_read2_b64 v[238:241], v87 offset0:120 offset1:128
	ds_read_b64 v[154:155], v204 offset:25376
	s_waitcnt lgkmcnt(2)
	v_mfma_f32_16x16x32_bf16 v[160:163], v[148:151], v[156:159], v[160:163]
	s_waitcnt lgkmcnt(1)
	v_mov_b32_e32 v152, v238
	v_mov_b32_e32 v153, v239
	ds_read_b64 v[86:87], v205 offset:32
	ds_read_b64 v[90:91], v205 offset:16928
	s_waitcnt lgkmcnt(2)
	v_mfma_f32_16x16x32_bf16 v[222:225], v[152:155], v[156:159], v[222:225]
	ds_read_b64 v[158:159], v205 offset:8480
	v_mov_b32_e32 v156, v232
	v_mov_b32_e32 v157, v233
	s_waitcnt lgkmcnt(2)
	v_mfma_f32_16x16x32_bf16 v[226:229], v[84:87], v[0:3], v[226:229]
	s_waitcnt lgkmcnt(0)
	v_mfma_f32_16x16x32_bf16 v[230:233], v[156:159], v[0:3], v[234:237]
	s_nop 5
	v_cvt_pk_bf16_f32 v198, v226, v227
	v_cvt_pk_bf16_f32 v199, v228, v229
	v_mfma_f32_16x16x32_bf16 v[234:237], v[88:91], v[0:3], v[160:163]
	s_nop 2
	ds_read_b64 v[162:163], v205 offset:25376
	v_mov_b32_e32 v160, v240
	v_mov_b32_e32 v161, v241
	v_mfma_f32_16x16x32_bf16 v[226:229], v[12:15], v[168:171], 0
	s_waitcnt lgkmcnt(0)
	v_mfma_f32_16x16x32_bf16 v[222:225], v[160:163], v[0:3], v[222:225]
	v_lshl_add_u64 v[0:1], v[180:181], 0, s[30:31]
	global_store_dwordx2 v[0:1], v[198:199], off
	v_cvt_pk_bf16_f32 v198, v230, v231
	v_cvt_pk_bf16_f32 v199, v232, v233
	global_store_dwordx2 v[0:1], v[198:199], off offset:32
	v_cvt_pk_bf16_f32 v198, v234, v235
	v_cvt_pk_bf16_f32 v199, v236, v237
	global_store_dwordx2 v[0:1], v[198:199], off offset:64
	v_cvt_pk_bf16_f32 v198, v222, v223
	v_cvt_pk_bf16_f32 v199, v224, v225
	global_store_dwordx2 v[0:1], v[198:199], off offset:96
	global_load_dword v3, v221, s[36:37] offset:4
	v_mfma_f32_16x16x32_bf16 v[222:225], v[4:7], v[168:171], 0
	v_mfma_f32_16x16x32_bf16 v[222:225], v[8:11], v[164:167], v[222:225]
	v_mfma_f32_16x16x32_bf16 v[230:233], v[20:23], v[168:171], 0
	v_mfma_f32_16x16x32_bf16 v[234:237], v[28:31], v[168:171], 0
	s_nop 5
	v_cndmask_b32_e64 v0, v216, v222, s[40:41]
	v_cndmask_b32_e64 v1, v216, v223, s[42:43]
	v_mfma_f32_16x16x32_bf16 v[238:241], v[36:39], v[168:171], 0
	v_mfma_f32_16x16x32_bf16 v[198:201], v[64:67], v[168:171], 0
	v_mfma_f32_16x16x32_bf16 v[168:171], v[72:75], v[168:171], 0
	v_mfma_f32_16x16x32_bf16 v[226:229], v[16:19], v[164:167], v[226:229]
	v_mfma_f32_16x16x32_bf16 v[230:233], v[24:27], v[164:167], v[230:233]
	v_mfma_f32_16x16x32_bf16 v[234:237], v[32:35], v[164:167], v[234:237]
	s_nop 5
	v_cndmask_b32_e64 v222, v216, v227, s[50:51]
	v_cndmask_b32_e64 v223, v216, v228, s[52:53]
	v_cndmask_b32_e64 v227, v216, v232, s[60:61]
	v_mfma_f32_16x16x32_bf16 v[238:241], v[40:43], v[164:167], v[238:241]
	v_cndmask_b32_e64 v228, v216, v233, s[62:63]
	v_cndmask_b32_e64 v232, v216, v237, s[70:71]
	v_cndmask_b32_e64 v237, v216, v242, s[80:81]
	v_mfma_f32_16x16x32_bf16 v[198:201], v[56:59], v[164:167], v[198:201]
	v_cndmask_b32_e64 v242, v216, v247, s[90:91]
	s_nop 2
	v_cndmask_b32_e64 v233, v216, v238, s[72:73]
	v_cndmask_b32_e64 v238, v216, v243, s[82:83]
	v_mfma_f32_16x16x32_bf16 v[164:167], v[68:71], v[164:167], v[168:171]
	v_cndmask_b32_e64 v243, v216, v248, s[92:93]
	v_cndmask_b32_e64 v247, v216, v200, s[4:5]
	v_cndmask_b32_e64 v248, v216, v201, s[6:7]
	v_max3_f32 v168, v0, s22, v1
	v_cndmask_b32_e64 v169, v216, v224, s[44:45]
	v_cndmask_b32_e64 v170, v216, v225, s[46:47]
	v_max3_f32 v168, v168, v169, v170
	v_cndmask_b32_e64 v171, v216, v226, s[48:49]
	v_max3_f32 v168, v168, v171, v222
	v_cndmask_b32_e64 v224, v216, v229, s[54:55]
	v_max3_f32 v168, v168, v223, v224
	v_cndmask_b32_e64 v225, v216, v230, s[56:57]
	v_cndmask_b32_e64 v226, v216, v231, s[58:59]
	v_max3_f32 v168, v168, v225, v226
	v_max3_f32 v168, v168, v227, v228
	v_cndmask_b32_e64 v229, v216, v234, s[64:65]
	v_cndmask_b32_e64 v230, v216, v235, s[66:67]
	v_max3_f32 v168, v168, v229, v230
	v_cndmask_b32_e64 v231, v216, v236, s[68:69]
	v_max3_f32 v168, v168, v231, v232
	v_cndmask_b32_e64 v234, v216, v239, s[74:75]
	v_max3_f32 v168, v168, v233, v234
	v_cndmask_b32_e64 v235, v216, v240, s[76:77]
	v_cndmask_b32_e64 v236, v216, v241, s[78:79]
	v_max3_f32 v168, v168, v235, v236
	v_max3_f32 v168, v168, v237, v238
	v_cndmask_b32_e64 v239, v216, v244, s[84:85]
	v_cndmask_b32_e64 v240, v216, v245, s[86:87]
	v_max3_f32 v168, v168, v239, v240
	v_cndmask_b32_e64 v241, v216, v246, s[88:89]
	v_max3_f32 v168, v168, v241, v242
	v_cndmask_b32_e64 v244, v216, v249, s[94:95]
	v_max3_f32 v168, v168, v243, v244
	v_cndmask_b32_e64 v245, v216, v198, s[96:97]
	v_cndmask_b32_e64 v246, v216, v199, s[2:3]
	v_max3_f32 v168, v168, v245, v246
	v_max3_f32 v168, v168, v247, v248
	v_cndmask_b32_e64 v249, v216, v164, s[8:9]
	v_cndmask_b32_e64 v252, v216, v165, s[10:11]
	v_max3_f32 v164, v168, v249, v252
	v_cndmask_b32_e64 v168, v216, v166, s[12:13]
	v_cndmask_b32_e64 v217, v216, v167, s[14:15]
	v_max3_f32 v164, v164, v168, v217
	v_mov_b32_e32 v166, v164
	s_nop 1
	v_permlane16_swap_b32_e32 v166, v164
	s_waitcnt vmcnt(0)
; __device__ __forceinline__ unsigned pk2(float lo, float hi) { f32x2_m v = {lo, hi}; bf16x2_m b = __builtin_convertvector(v, bf16x2_m); return __builtin_bit_cast(unsigned, b); }
; #define MFMA16(a, b, c) __builtin_amdgcn_mfma_f32_16x16x32_bf16(a, b, c, 0, 0, 0)
; __device__ __forceinline__ void swa_phase(const Ctx& C, const bf16* PROJ, const float* sinks, bf16* YSWA) {
;     ...
;             for (int j = 0; j < 9; ++j) { f32x4 a = {0.f, 0.f, 0.f, 0.f}; a = MFMA16(kf[j][0], qf[g][0], a); a = MFMA16(kf[j][1], qf[g][1], a); s[j] = a; }
;             const int qr = 16 * w + c16; float mx = -INFINITY;
; #pragma unroll
;             for (int j = 0; j < 9; ++j)
; #pragma unroll
;                 for (int r = 0; r < 4; ++r) { const int kr = 16 * w - 128 + 16 * j + 4 * g4 + r, diff = qr - kr; const bool ok = diff >= 0 && diff < 128 && (128 * n + kr) >= 0;
;                     s[j][r] = ok ? s[j][r] : -INFINITY; mx = fmaxf(mx, s[j][r]); }
;             mx = fmaxf(mx, __shfl_xor(mx, 16)); mx = fmaxf(mx, __shfl_xor(mx, 32)); mx = fmaxf(mx, sink2);
;             float sum = 0.f;
; #pragma unroll
;             for (int j = 0; j < 9; ++j)
; #pragma unroll
;                 for (int r = 0; r < 4; ++r) { const float e = __builtin_amdgcn_exp2f(s[j][r] - mx); s[j][r] = e; sum += e; }
;             sum += __shfl_xor(sum, 16); sum += __shfl_xor(sum, 32); sum += __builtin_amdgcn_exp2f(sink2 - mx);
;             const float inv = 1.0f / sum;
;             unsigned pw[10][2];
; #pragma unroll
;             for (int j = 0; j < 9; ++j) { pw[j][0] = pk2(s[j][0] * inv, s[j][1] * inv); pw[j][1] = pk2(s[j][2] * inv, s[j][3] * inv); }
	v_mul_f32_e32 v165, 0x3fb8aa3b, v3
	v_mfma_f32_16x16x32_bf16 v[4:7], v[4:7], v[80:83], 0
	s_waitcnt lgkmcnt(0)
	v_max_f32_e32 v166, v166, v166
	v_max_f32_e32 v164, v164, v166
	v_mov_b32_e32 v166, v164
	s_nop 1
	v_permlane32_swap_b32_e32 v166, v164
	v_mfma_f32_16x16x32_bf16 v[4:7], v[8:11], v[76:79], v[4:7]
	s_waitcnt lgkmcnt(0)
	v_max3_f32 v207, v164, v166, v165
	v_sub_f32_e32 v164, v169, v207
	v_sub_f32_e32 v169, v223, v207
	v_exp_f32_e32 v198, v169
	v_sub_f32_e32 v169, v224, v207
	v_exp_f32_e32 v199, v169
	v_sub_f32_e32 v169, v225, v207
	v_exp_f32_e32 v200, v169
	v_sub_f32_e32 v169, v226, v207
	v_exp_f32_e32 v201, v169
	v_sub_f32_e32 v169, v227, v207
	v_sub_f32_e32 v167, v222, v207
	v_exp_f32_e32 v222, v169
	v_sub_f32_e32 v169, v228, v207
	v_exp_f32_e32 v223, v169
	v_sub_f32_e32 v169, v229, v207
	v_exp_f32_e32 v224, v169
	v_sub_f32_e32 v169, v230, v207
	v_exp_f32_e32 v225, v169
	v_sub_f32_e32 v169, v231, v207
	v_exp_f32_e32 v226, v169
	v_sub_f32_e32 v169, v232, v207
	v_exp_f32_e32 v227, v169
	v_sub_f32_e32 v169, v233, v207
	v_exp_f32_e32 v228, v169
	v_sub_f32_e32 v169, v234, v207
	v_exp_f32_e32 v229, v169
	v_sub_f32_e32 v169, v235, v207
	v_exp_f32_e32 v230, v169
	v_sub_f32_e32 v169, v236, v207
	v_exp_f32_e32 v231, v169
	v_sub_f32_e32 v169, v237, v207
	v_exp_f32_e32 v232, v169
	v_sub_f32_e32 v169, v238, v207
	v_exp_f32_e32 v233, v169
	v_sub_f32_e32 v169, v239, v207
	v_exp_f32_e32 v234, v169
	v_sub_f32_e32 v169, v240, v207
	v_exp_f32_e32 v235, v169
	v_sub_f32_e32 v169, v241, v207
	v_sub_f32_e32 v0, v0, v207
	v_exp_f32_e32 v236, v169
	v_sub_f32_e32 v169, v242, v207
	v_exp_f32_e32 v0, v0
	v_sub_f32_e32 v1, v1, v207
	v_exp_f32_e32 v237, v169
	v_sub_f32_e32 v169, v243, v207
	v_exp_f32_e32 v1, v1
	v_exp_f32_e32 v238, v169
	v_sub_f32_e32 v169, v244, v207
	v_exp_f32_e32 v164, v164
	v_sub_f32_e32 v165, v170, v207
	v_exp_f32_e32 v239, v169
	v_sub_f32_e32 v169, v245, v207
	v_sub_f32_e32 v168, v168, v207
	v_exp_f32_e32 v165, v165
	v_sub_f32_e32 v166, v171, v207
	v_exp_f32_e32 v240, v169
	v_sub_f32_e32 v169, v246, v207
	v_exp_f32_e32 v246, v168
	v_sub_f32_e32 v168, v217, v207
	v_exp_f32_e32 v166, v166
	v_exp_f32_e32 v241, v169
	v_sub_f32_e32 v169, v247, v207
	v_exp_f32_e32 v247, v168
	v_add_f32_e32 v168, 0, v0
	v_exp_f32_e32 v167, v167
	v_add_f32_e32 v168, v1, v168
	v_add_f32_e32 v168, v164, v168
	v_add_f32_e32 v168, v165, v168
	v_add_f32_e32 v168, v166, v168
	v_add_f32_e32 v168, v167, v168
	v_add_f32_e32 v168, v198, v168
	v_add_f32_e32 v168, v199, v168
	v_add_f32_e32 v168, v200, v168
	v_add_f32_e32 v168, v201, v168
	v_add_f32_e32 v168, v222, v168
	v_add_f32_e32 v168, v223, v168
	v_add_f32_e32 v168, v224, v168
	v_add_f32_e32 v168, v225, v168
	v_add_f32_e32 v168, v226, v168
	v_add_f32_e32 v168, v227, v168
	v_add_f32_e32 v168, v228, v168
	v_add_f32_e32 v168, v229, v168
	v_add_f32_e32 v168, v230, v168
	v_add_f32_e32 v168, v231, v168
	v_add_f32_e32 v168, v232, v168
	v_add_f32_e32 v168, v233, v168
	v_add_f32_e32 v168, v234, v168
	v_add_f32_e32 v168, v235, v168
	v_add_f32_e32 v168, v236, v168
	v_add_f32_e32 v168, v237, v168
	v_exp_f32_e32 v242, v169
	v_sub_f32_e32 v169, v248, v207
	v_add_f32_e32 v168, v238, v168
	v_exp_f32_e32 v243, v169
	v_sub_f32_e32 v169, v249, v207
	v_add_f32_e32 v168, v239, v168
	v_exp_f32_e32 v244, v169
	v_sub_f32_e32 v169, v252, v207
	v_add_f32_e32 v168, v240, v168
	v_exp_f32_e32 v245, v169
	v_add_f32_e32 v168, v241, v168
	v_add_f32_e32 v168, v242, v168
	v_add_f32_e32 v168, v243, v168
	v_add_f32_e32 v168, v244, v168
	v_add_f32_e32 v168, v245, v168
	v_add_f32_e32 v168, v246, v168
	v_add_f32_e32 v168, v247, v168
	v_mov_b32_e32 v169, v168
	s_nop 1
	v_permlane16_swap_b32_e32 v169, v168
	v_fma_f32 v3, v3, s23, -v207
	v_exp_f32_e32 v3, v3
	v_mfma_f32_16x16x32_bf16 v[8:11], v[12:15], v[80:83], 0
	s_waitcnt lgkmcnt(0)
	v_add_f32_e32 v168, v168, v169
	v_mov_b32_e32 v169, v168
	s_nop 1
	v_permlane32_swap_b32_e32 v169, v168
	v_mfma_f32_16x16x32_bf16 v[12:15], v[20:23], v[80:83], 0
	s_waitcnt lgkmcnt(0)
	v_add_f32_e32 v168, v168, v169
	v_add_f32_e32 v3, v3, v168
	v_div_scale_f32 v168, s[20:21], v3, v3, 1.0
	v_rcp_f32_e32 v169, v168
	v_mfma_f32_16x16x32_bf16 v[8:11], v[16:19], v[76:79], v[8:11]
	v_fma_f32 v170, -v168, v169, 1.0
	v_fmac_f32_e32 v169, v170, v169
	v_div_scale_f32 v170, vcc, 1.0, v3, 1.0
	v_mul_f32_e32 v171, v170, v169
	v_fma_f32 v207, -v168, v171, v170
	v_fmac_f32_e32 v171, v207, v169
	v_fma_f32 v168, -v168, v171, v170
	v_div_fmas_f32 v168, v168, v169, v171
	v_div_fixup_f32 v248, v168, v3, 1.0
	v_pk_mul_f32 v[0:1], v[0:1], v[248:249] op_sel_hi:[1,0]
	v_mov_b32_e32 v3, v2
	v_cvt_pk_bf16_f32 v168, v0, v1
	v_pk_mul_f32 v[0:1], v[164:165], v[248:249] op_sel_hi:[1,0]
	v_mfma_f32_16x16x32_bf16 v[16:19], v[28:31], v[80:83], 0
	v_cvt_pk_bf16_f32 v169, v0, v1
	v_pk_mul_f32 v[0:1], v[166:167], v[248:249] op_sel_hi:[1,0]
	s_nop 0
	v_cvt_pk_bf16_f32 v170, v0, v1
	v_pk_mul_f32 v[0:1], v[198:199], v[248:249] op_sel_hi:[1,0]
	v_mfma_f32_16x16x32_bf16 v[12:15], v[24:27], v[76:79], v[12:15]
	v_cvt_pk_bf16_f32 v171, v0, v1
	v_pk_mul_f32 v[0:1], v[200:201], v[248:249] op_sel_hi:[1,0]
	s_nop 0
	v_cvt_pk_bf16_f32 v198, v0, v1
	v_pk_mul_f32 v[0:1], v[222:223], v[248:249] op_sel_hi:[1,0]
	v_mfma_f32_16x16x32_bf16 v[20:23], v[36:39], v[80:83], 0
	v_cvt_pk_bf16_f32 v199, v0, v1
	v_pk_mul_f32 v[0:1], v[224:225], v[248:249] op_sel_hi:[1,0]
	s_nop 0
	v_cvt_pk_bf16_f32 v200, v0, v1
	v_pk_mul_f32 v[0:1], v[226:227], v[248:249] op_sel_hi:[1,0]
	v_pk_mul_f32 v[226:227], v[246:247], v[248:249] op_sel_hi:[1,0]
	v_cvt_pk_bf16_f32 v201, v0, v1
	v_pk_mul_f32 v[0:1], v[228:229], v[248:249] op_sel_hi:[1,0]
	v_mfma_f32_16x16x32_bf16 v[16:19], v[32:35], v[76:79], v[16:19]
; #define LAS __attribute__((address_space(3)))
; __device__ __forceinline__ void swa_phase(const Ctx& C, const bf16* PROJ, const float* sinks, bf16* YSWA) {
;     ...
;             for (int j = 0; j < 9; ++j) { f32x4 a = {0.f, 0.f, 0.f, 0.f}; a = MFMA16(kf[j][0], qf[g][0], a); a = MFMA16(kf[j][1], qf[g][1], a); s[j] = a; }
;             const int qr = 16 * w + c16; float mx = -INFINITY;
; #pragma unroll
;             for (int j = 0; j < 9; ++j)
; #pragma unroll
;                 for (int r = 0; r < 4; ++r) { const int kr = 16 * w - 128 + 16 * j + 4 * g4 + r, diff = qr - kr; const bool ok = diff >= 0 && diff < 128 && (128 * n + kr) >= 0;
;                     s[j][r] = ok ? s[j][r] : -INFINITY; mx = fmaxf(mx, s[j][r]); }
;             mx = fmaxf(mx, __shfl_xor(mx, 16)); mx = fmaxf(mx, __shfl_xor(mx, 32)); mx = fmaxf(mx, sink2);
;             float sum = 0.f;
; #pragma unroll
;             for (int j = 0; j < 9; ++j)
; #pragma unroll
;                 for (int r = 0; r < 4; ++r) { const float e = __builtin_amdgcn_exp2f(s[j][r] - mx); s[j][r] = e; sum += e; }
;             sum += __shfl_xor(sum, 16); sum += __shfl_xor(sum, 32); sum += __builtin_amdgcn_exp2f(sink2 - mx);
;             const float inv = 1.0f / sum;
;             unsigned pw[10][2];
; #pragma unroll
;             for (int j = 0; j < 9; ++j) { pw[j][0] = pk2(s[j][0] * inv, s[j][1] * inv); pw[j][1] = pk2(s[j][2] * inv, s[j][3] * inv); }
;             pw[9][0] = 0u; pw[9][1] = 0u;
;             f32x4 o[4];
; #pragma unroll
;             for (int dt = 0; dt < 4; ++dt) o[dt] = (f32x4){0.f, 0.f, 0.f, 0.f};
; #pragma unroll
;             for (int sI = 0; sI < 5; ++sI) {
;                 const v4u pb = {pw[2 * sI][0], pw[2 * sI][1], pw[2 * sI + 1][0], pw[2 * sI + 1][1]};
;                 const int kkA = 16 * w + 32 * sI + 4 * g4; int kkB = kkA + 16; if (kkB > 252) kkB = 252;
; #pragma unroll
;                 for (int dt = 0; dt < 4; ++dt) { const LAS bf16* vp = vt + (16 * dt + c16) * 264;
;                     const v2u va = *(const LAS v2u*)(vp + kkA), vb = *(const LAS v2u*)(vp + kkB);
;                     const v4u av = {va.x, va.y, vb.x, vb.y};
;                     o[dt] = MFMA16(__builtin_bit_cast(bf16x8, av), __builtin_bit_cast(bf16x8, pb), o[dt]); }
;             }
;             bf16* op = YSWA + (size_t)(q0 + c16) * 768 + 64 * h + 4 * g4;
; #pragma unroll
	v_cvt_pk_bf16_f32 v222, v0, v1
	v_pk_mul_f32 v[0:1], v[230:231], v[248:249] op_sel_hi:[1,0]
	s_nop 0
	v_cvt_pk_bf16_f32 v223, v0, v1
	v_pk_mul_f32 v[0:1], v[232:233], v[248:249] op_sel_hi:[1,0]
	v_mfma_f32_16x16x32_bf16 v[230:233], v[96:99], v[168:171], 0
	v_cvt_pk_bf16_f32 v224, v0, v1
	v_pk_mul_f32 v[0:1], v[234:235], v[248:249] op_sel_hi:[1,0]
	s_nop 0
	v_cvt_pk_bf16_f32 v225, v0, v1
	v_pk_mul_f32 v[0:1], v[236:237], v[248:249] op_sel_hi:[1,0]
	v_mfma_f32_16x16x32_bf16 v[234:237], v[100:103], v[168:171], 0
	v_cvt_pk_bf16_f32 v164, v0, v1
	v_pk_mul_f32 v[0:1], v[238:239], v[248:249] op_sel_hi:[1,0]
	s_nop 0
	v_cvt_pk_bf16_f32 v165, v0, v1
	v_pk_mul_f32 v[0:1], v[240:241], v[248:249] op_sel_hi:[1,0]
	v_mfma_f32_16x16x32_bf16 v[230:233], v[112:115], v[198:201], v[230:233]
	v_cvt_pk_bf16_f32 v166, v0, v1
	v_pk_mul_f32 v[0:1], v[242:243], v[248:249] op_sel_hi:[1,0]
	s_nop 0
	v_cvt_pk_bf16_f32 v167, v0, v1
	v_pk_mul_f32 v[0:1], v[244:245], v[248:249] op_sel_hi:[1,0]
	v_mfma_f32_16x16x32_bf16 v[234:237], v[116:119], v[198:201], v[234:237]
	v_cvt_pk_bf16_f32 v0, v0, v1
	v_cvt_pk_bf16_f32 v1, v226, v227
	v_mfma_f32_16x16x32_bf16 v[226:229], v[92:95], v[168:171], 0
	v_mfma_f32_16x16x32_bf16 v[168:171], v[104:107], v[168:171], 0
	v_mfma_f32_16x16x32_bf16 v[226:229], v[108:111], v[198:201], v[226:229]
	v_mfma_f32_16x16x32_bf16 v[168:171], v[120:123], v[198:201], v[168:171]
	v_mfma_f32_16x16x32_bf16 v[198:201], v[124:127], v[222:225], v[226:229]
	v_mfma_f32_16x16x32_bf16 v[226:229], v[128:131], v[222:225], v[230:233]
	v_mfma_f32_16x16x32_bf16 v[230:233], v[132:135], v[222:225], v[234:237]
	v_mfma_f32_16x16x32_bf16 v[168:171], v[136:139], v[222:225], v[168:171]
	v_mfma_f32_16x16x32_bf16 v[198:201], v[140:143], v[164:167], v[198:201]
	v_mfma_f32_16x16x32_bf16 v[222:225], v[144:147], v[164:167], v[226:229]
	v_mfma_f32_16x16x32_bf16 v[226:229], v[148:151], v[164:167], v[230:233]
	v_mfma_f32_16x16x32_bf16 v[164:167], v[152:155], v[164:167], v[168:171]
	v_mfma_f32_16x16x32_bf16 v[168:171], v[84:87], v[0:3], v[198:201]
	v_mfma_f32_16x16x32_bf16 v[198:201], v[156:159], v[0:3], v[222:225]
	v_mfma_f32_16x16x32_bf16 v[222:225], v[88:91], v[0:3], v[226:229]
	s_nop 5
	v_cvt_pk_bf16_f32 v168, v168, v169
	v_cvt_pk_bf16_f32 v169, v170, v171
	v_mfma_f32_16x16x32_bf16 v[164:167], v[160:163], v[0:3], v[164:167]
	v_lshl_add_u64 v[0:1], v[180:181], 0, s[26:27]
	global_store_dwordx2 v[0:1], v[168:169], off
	v_cvt_pk_bf16_f32 v168, v198, v199
	v_cvt_pk_bf16_f32 v169, v200, v201
	global_store_dwordx2 v[0:1], v[168:169], off offset:32
	v_cvt_pk_bf16_f32 v168, v222, v223
	v_cvt_pk_bf16_f32 v169, v224, v225
	s_nop 0
	v_cvt_pk_bf16_f32 v164, v164, v165
	v_cvt_pk_bf16_f32 v165, v166, v167
	global_store_dwordx2 v[0:1], v[168:169], off offset:64
	global_store_dwordx2 v[0:1], v[164:165], off offset:96
	global_load_dword v3, v221, s[36:37] offset:8
	v_cndmask_b32_e64 v0, v216, v4, s[40:41]
	v_cndmask_b32_e64 v1, v216, v5, s[42:43]
	v_max3_f32 v4, v0, s22, v1
	v_cndmask_b32_e64 v5, v216, v6, s[44:45]
	v_cndmask_b32_e64 v6, v216, v7, s[46:47]
	v_mfma_f32_16x16x32_bf16 v[24:27], v[44:47], v[80:83], 0
	v_max3_f32 v4, v4, v5, v6
	v_cndmask_b32_e64 v7, v216, v8, s[48:49]
	v_cndmask_b32_e64 v8, v216, v9, s[50:51]
	v_max3_f32 v4, v4, v7, v8
	v_cndmask_b32_e64 v9, v216, v10, s[52:53]
	v_cndmask_b32_e64 v10, v216, v11, s[54:55]
	v_mfma_f32_16x16x32_bf16 v[20:23], v[40:43], v[76:79], v[20:23]
	v_max3_f32 v4, v4, v9, v10
	v_cndmask_b32_e64 v11, v216, v12, s[56:57]
	v_cndmask_b32_e64 v40, v216, v13, s[58:59]
	v_mfma_f32_16x16x32_bf16 v[28:31], v[60:63], v[80:83], 0
	v_max3_f32 v4, v4, v11, v40
	v_cndmask_b32_e64 v41, v216, v14, s[60:61]
	v_cndmask_b32_e64 v42, v216, v15, s[62:63]
	v_mfma_f32_16x16x32_bf16 v[24:27], v[48:51], v[76:79], v[24:27]
	v_max3_f32 v4, v4, v41, v42
	v_cndmask_b32_e64 v43, v216, v16, s[64:65]
	v_cndmask_b32_e64 v44, v216, v17, s[66:67]
	v_mfma_f32_16x16x32_bf16 v[32:35], v[64:67], v[80:83], 0
	v_max3_f32 v4, v4, v43, v44
	v_cndmask_b32_e64 v45, v216, v18, s[68:69]
	v_cndmask_b32_e64 v46, v216, v19, s[70:71]
	v_mfma_f32_16x16x32_bf16 v[28:31], v[52:55], v[76:79], v[28:31]
	v_max3_f32 v4, v4, v45, v46
	v_cndmask_b32_e64 v47, v216, v20, s[72:73]
	v_cndmask_b32_e64 v48, v216, v21, s[74:75]
	v_mfma_f32_16x16x32_bf16 v[36:39], v[72:75], v[80:83], 0
	v_max3_f32 v4, v4, v47, v48
	v_cndmask_b32_e64 v49, v216, v22, s[76:77]
	v_cndmask_b32_e64 v50, v216, v23, s[78:79]
	v_mfma_f32_16x16x32_bf16 v[32:35], v[56:59], v[76:79], v[32:35]
	v_max3_f32 v4, v4, v49, v50
	v_cndmask_b32_e64 v51, v216, v24, s[80:81]
	v_cndmask_b32_e64 v52, v216, v25, s[82:83]
	v_max3_f32 v4, v4, v51, v52
	v_cndmask_b32_e64 v53, v216, v26, s[84:85]
	v_cndmask_b32_e64 v54, v216, v27, s[86:87]
	v_mfma_f32_16x16x32_bf16 v[36:39], v[68:71], v[76:79], v[36:39]
	v_max3_f32 v4, v4, v53, v54
	v_cndmask_b32_e64 v55, v216, v28, s[88:89]
	v_cndmask_b32_e64 v56, v216, v29, s[90:91]
	v_max3_f32 v4, v4, v55, v56
	v_cndmask_b32_e64 v57, v216, v30, s[92:93]
	v_cndmask_b32_e64 v58, v216, v31, s[94:95]
	v_max3_f32 v4, v4, v57, v58
	v_cndmask_b32_e64 v59, v216, v32, s[96:97]
	v_cndmask_b32_e64 v60, v216, v33, s[2:3]
	v_max3_f32 v4, v4, v59, v60
	v_cndmask_b32_e64 v61, v216, v34, s[4:5]
	v_cndmask_b32_e64 v62, v216, v35, s[6:7]
	v_max3_f32 v4, v4, v61, v62
	v_cndmask_b32_e64 v63, v216, v36, s[8:9]
	v_cndmask_b32_e64 v64, v216, v37, s[10:11]
	v_max3_f32 v4, v4, v63, v64
	v_cndmask_b32_e64 v65, v216, v38, s[12:13]
	v_cndmask_b32_e64 v66, v216, v39, s[14:15]
	v_max3_f32 v4, v4, v65, v66
	v_mov_b32_e32 v13, v4
	s_nop 1
	v_permlane16_swap_b32_e32 v13, v4
	s_waitcnt lgkmcnt(0)
; __device__ __forceinline__ void swa_phase(const Ctx& C, const bf16* PROJ, const float* sinks, bf16* YSWA) {
;     ...
;             mx = fmaxf(mx, __shfl_xor(mx, 16)); mx = fmaxf(mx, __shfl_xor(mx, 32)); mx = fmaxf(mx, sink2);
;             float sum = 0.f;
; #pragma unroll
;             for (int j = 0; j < 9; ++j)
; #pragma unroll
;                 for (int r = 0; r < 4; ++r) { const float e = __builtin_amdgcn_exp2f(s[j][r] - mx); s[j][r] = e; sum += e; }
;             sum += __shfl_xor(sum, 16); sum += __shfl_xor(sum, 32); sum += __builtin_amdgcn_exp2f(sink2 - mx);
	v_max_f32_e32 v13, v13, v13
	v_max_f32_e32 v4, v4, v13
	v_mov_b32_e32 v13, v4
	s_nop 1
	v_permlane32_swap_b32_e32 v13, v4
	s_waitcnt vmcnt(0)
	v_mul_f32_e32 v12, 0x3fb8aa3b, v3
	s_waitcnt lgkmcnt(0)
	v_max3_f32 v67, v4, v13, v12
	v_sub_f32_e32 v4, v5, v67
	v_sub_f32_e32 v5, v6, v67
	v_sub_f32_e32 v6, v7, v67
	v_sub_f32_e32 v7, v8, v67
	v_sub_f32_e32 v8, v9, v67
	v_exp_f32_e32 v12, v8
	v_sub_f32_e32 v8, v10, v67
	v_exp_f32_e32 v13, v8
	v_sub_f32_e32 v8, v11, v67
	v_exp_f32_e32 v14, v8
	v_sub_f32_e32 v8, v40, v67
	v_exp_f32_e32 v15, v8
	v_sub_f32_e32 v8, v41, v67
	v_exp_f32_e32 v16, v8
	v_sub_f32_e32 v8, v42, v67
	v_exp_f32_e32 v17, v8
	v_sub_f32_e32 v8, v43, v67
	v_exp_f32_e32 v18, v8
	v_sub_f32_e32 v8, v44, v67
	v_exp_f32_e32 v19, v8
	v_sub_f32_e32 v8, v45, v67
	v_exp_f32_e32 v20, v8
	v_sub_f32_e32 v8, v46, v67
	v_exp_f32_e32 v21, v8
	v_sub_f32_e32 v8, v47, v67
	v_exp_f32_e32 v22, v8
	v_sub_f32_e32 v8, v48, v67
	v_exp_f32_e32 v23, v8
	v_sub_f32_e32 v8, v49, v67
	v_exp_f32_e32 v24, v8
	v_sub_f32_e32 v8, v50, v67
	v_exp_f32_e32 v25, v8
	v_sub_f32_e32 v8, v51, v67
	v_exp_f32_e32 v26, v8
	v_sub_f32_e32 v8, v52, v67
	v_exp_f32_e32 v27, v8
	v_sub_f32_e32 v8, v53, v67
	v_exp_f32_e32 v28, v8
	v_sub_f32_e32 v8, v54, v67
	v_exp_f32_e32 v29, v8
	v_sub_f32_e32 v8, v55, v67
	v_exp_f32_e32 v30, v8
	v_sub_f32_e32 v8, v56, v67
	v_exp_f32_e32 v31, v8
	v_sub_f32_e32 v8, v57, v67
	v_exp_f32_e32 v32, v8
	v_sub_f32_e32 v8, v58, v67
	v_exp_f32_e32 v33, v8
	v_sub_f32_e32 v8, v59, v67
	v_exp_f32_e32 v34, v8
	v_sub_f32_e32 v8, v60, v67
	v_exp_f32_e32 v35, v8
	v_sub_f32_e32 v8, v61, v67
	v_sub_f32_e32 v0, v0, v67
	v_exp_f32_e32 v36, v8
	v_sub_f32_e32 v8, v62, v67
	v_exp_f32_e32 v0, v0
	v_sub_f32_e32 v1, v1, v67
	v_exp_f32_e32 v37, v8
	v_sub_f32_e32 v8, v63, v67
	v_exp_f32_e32 v1, v1
	v_exp_f32_e32 v38, v8
	v_sub_f32_e32 v8, v64, v67
	v_exp_f32_e32 v4, v4
	v_exp_f32_e32 v39, v8
	v_sub_f32_e32 v8, v65, v67
	v_exp_f32_e32 v5, v5
	v_exp_f32_e32 v40, v8
	v_sub_f32_e32 v8, v66, v67
	v_exp_f32_e32 v6, v6
	v_exp_f32_e32 v41, v8
	v_add_f32_e32 v8, 0, v0
	v_exp_f32_e32 v7, v7
	v_add_f32_e32 v8, v1, v8
	v_add_f32_e32 v8, v4, v8
	v_add_f32_e32 v8, v5, v8
	v_add_f32_e32 v8, v6, v8
	v_add_f32_e32 v8, v7, v8
	v_add_f32_e32 v8, v12, v8
	v_add_f32_e32 v8, v13, v8
	v_add_f32_e32 v8, v14, v8
	v_add_f32_e32 v8, v15, v8
	v_add_f32_e32 v8, v16, v8
	v_add_f32_e32 v8, v17, v8
	v_add_f32_e32 v8, v18, v8
	v_add_f32_e32 v8, v19, v8
	v_add_f32_e32 v8, v20, v8
	v_add_f32_e32 v8, v21, v8
	v_add_f32_e32 v8, v22, v8
	v_add_f32_e32 v8, v23, v8
	v_add_f32_e32 v8, v24, v8
	v_add_f32_e32 v8, v25, v8
	v_add_f32_e32 v8, v26, v8
	v_add_f32_e32 v8, v27, v8
	v_add_f32_e32 v8, v28, v8
	v_add_f32_e32 v8, v29, v8
	v_add_f32_e32 v8, v30, v8
	v_add_f32_e32 v8, v31, v8
	v_add_f32_e32 v8, v32, v8
	v_add_f32_e32 v8, v33, v8
	v_add_f32_e32 v8, v34, v8
	v_add_f32_e32 v8, v35, v8
	v_add_f32_e32 v8, v36, v8
	v_add_f32_e32 v8, v37, v8
	v_add_f32_e32 v8, v38, v8
	v_add_f32_e32 v8, v39, v8
	v_add_f32_e32 v8, v40, v8
	v_add_f32_e32 v8, v41, v8
	v_mov_b32_e32 v9, v8
	s_nop 1
	v_permlane16_swap_b32_e32 v9, v8
	v_fma_f32 v3, v3, s23, -v67
	v_exp_f32_e32 v3, v3
	s_waitcnt lgkmcnt(0)
	v_add_f32_e32 v8, v8, v9
	v_mov_b32_e32 v9, v8
	s_nop 1
	v_permlane32_swap_b32_e32 v9, v8
	s_waitcnt lgkmcnt(0)
; #define GAS __attribute__((address_space(1)))
; #define LAS __attribute__((address_space(3)))
; __device__ __forceinline__ unsigned pk2(float lo, float hi) { f32x2_m v = {lo, hi}; bf16x2_m b = __builtin_convertvector(v, bf16x2_m); return __builtin_bit_cast(unsigned, b); }
; #define MFMA16(a, b, c) __builtin_amdgcn_mfma_f32_16x16x32_bf16(a, b, c, 0, 0, 0)
; __device__ __forceinline__ void swa_phase(const Ctx& C, const bf16* PROJ, const float* sinks, bf16* YSWA) {
;     ...
;     for (int u = C.vcu; u < 512; u += C.G) {
;     ...
;             const float inv = 1.0f / sum;
;             unsigned pw[10][2];
; #pragma unroll
;             for (int j = 0; j < 9; ++j) { pw[j][0] = pk2(s[j][0] * inv, s[j][1] * inv); pw[j][1] = pk2(s[j][2] * inv, s[j][3] * inv); }
;             pw[9][0] = 0u; pw[9][1] = 0u;
;             f32x4 o[4];
; #pragma unroll
;             for (int dt = 0; dt < 4; ++dt) o[dt] = (f32x4){0.f, 0.f, 0.f, 0.f};
; #pragma unroll
;             for (int sI = 0; sI < 5; ++sI) {
;                 const v4u pb = {pw[2 * sI][0], pw[2 * sI][1], pw[2 * sI + 1][0], pw[2 * sI + 1][1]};
;                 const int kkA = 16 * w + 32 * sI + 4 * g4; int kkB = kkA + 16; if (kkB > 252) kkB = 252;
; #pragma unroll
;                 for (int dt = 0; dt < 4; ++dt) { const LAS bf16* vp = vt + (16 * dt + c16) * 264;
;                     const v2u va = *(const LAS v2u*)(vp + kkA), vb = *(const LAS v2u*)(vp + kkB);
;                     const v4u av = {va.x, va.y, vb.x, vb.y};
;                     o[dt] = MFMA16(__builtin_bit_cast(bf16x8, av), __builtin_bit_cast(bf16x8, pb), o[dt]); }
;             }
;             bf16* op = YSWA + (size_t)(q0 + c16) * 768 + 64 * h + 4 * g4;
; #pragma unroll
;             for (int dt = 0; dt < 4; ++dt) { v2u wv; wv.x = pk2(o[dt][0], o[dt][1]); wv.y = pk2(o[dt][2], o[dt][3]); *(GAS v2u*)(op + 16 * dt) = wv; }
	v_add_f32_e32 v8, v8, v9
	v_add_f32_e32 v3, v3, v8
	v_div_scale_f32 v8, s[20:21], v3, v3, 1.0
	v_rcp_f32_e32 v9, v8
	s_add_i32 s20, s19, 0x100
	s_cmpk_lt_i32 s19, 0x100
	s_mov_b32 s19, s20
	v_fma_f32 v10, -v8, v9, 1.0
	v_fmac_f32_e32 v9, v10, v9
	v_div_scale_f32 v10, vcc, 1.0, v3, 1.0
	v_mul_f32_e32 v11, v10, v9
	v_fma_f32 v42, -v8, v11, v10
	v_fmac_f32_e32 v11, v42, v9
	v_fma_f32 v8, -v8, v11, v10
	v_div_fmas_f32 v8, v8, v9, v11
	v_div_fixup_f32 v42, v8, v3, 1.0
	v_pk_mul_f32 v[0:1], v[0:1], v[42:43] op_sel_hi:[1,0]
	v_mov_b32_e32 v3, v2
	v_cvt_pk_bf16_f32 v8, v0, v1
	v_pk_mul_f32 v[0:1], v[4:5], v[42:43] op_sel_hi:[1,0]
	s_nop 0
	v_cvt_pk_bf16_f32 v9, v0, v1
	v_pk_mul_f32 v[0:1], v[6:7], v[42:43] op_sel_hi:[1,0]
	s_nop 0
	v_cvt_pk_bf16_f32 v10, v0, v1
	v_pk_mul_f32 v[0:1], v[12:13], v[42:43] op_sel_hi:[1,0]
	s_nop 0
	v_cvt_pk_bf16_f32 v11, v0, v1
	v_pk_mul_f32 v[0:1], v[14:15], v[42:43] op_sel_hi:[1,0]
	s_nop 0
	v_cvt_pk_bf16_f32 v12, v0, v1
	v_pk_mul_f32 v[0:1], v[16:17], v[42:43] op_sel_hi:[1,0]
	s_nop 0
	v_cvt_pk_bf16_f32 v13, v0, v1
	v_pk_mul_f32 v[0:1], v[18:19], v[42:43] op_sel_hi:[1,0]
	s_nop 0
	v_cvt_pk_bf16_f32 v14, v0, v1
	v_pk_mul_f32 v[0:1], v[20:21], v[42:43] op_sel_hi:[1,0]
	v_pk_mul_f32 v[20:21], v[40:41], v[42:43] op_sel_hi:[1,0]
	v_cvt_pk_bf16_f32 v15, v0, v1
	v_pk_mul_f32 v[0:1], v[22:23], v[42:43] op_sel_hi:[1,0]
	s_nop 0
	v_cvt_pk_bf16_f32 v16, v0, v1
	v_pk_mul_f32 v[0:1], v[24:25], v[42:43] op_sel_hi:[1,0]
	s_nop 0
	v_cvt_pk_bf16_f32 v17, v0, v1
	v_pk_mul_f32 v[0:1], v[26:27], v[42:43] op_sel_hi:[1,0]
	v_mfma_f32_16x16x32_bf16 v[24:27], v[96:99], v[8:11], 0
	v_cvt_pk_bf16_f32 v18, v0, v1
	v_pk_mul_f32 v[0:1], v[28:29], v[42:43] op_sel_hi:[1,0]
	s_nop 0
	v_cvt_pk_bf16_f32 v19, v0, v1
	v_pk_mul_f32 v[0:1], v[30:31], v[42:43] op_sel_hi:[1,0]
	v_mfma_f32_16x16x32_bf16 v[28:31], v[100:103], v[8:11], 0
	v_cvt_pk_bf16_f32 v4, v0, v1
	v_pk_mul_f32 v[0:1], v[32:33], v[42:43] op_sel_hi:[1,0]
	s_nop 0
	v_cvt_pk_bf16_f32 v5, v0, v1
	v_pk_mul_f32 v[0:1], v[34:35], v[42:43] op_sel_hi:[1,0]
	v_mfma_f32_16x16x32_bf16 v[24:27], v[112:115], v[12:15], v[24:27]
	v_cvt_pk_bf16_f32 v6, v0, v1
	v_pk_mul_f32 v[0:1], v[36:37], v[42:43] op_sel_hi:[1,0]
	s_nop 0
	v_cvt_pk_bf16_f32 v7, v0, v1
	v_pk_mul_f32 v[0:1], v[38:39], v[42:43] op_sel_hi:[1,0]
	v_mfma_f32_16x16x32_bf16 v[28:31], v[116:119], v[12:15], v[28:31]
	v_cvt_pk_bf16_f32 v0, v0, v1
	v_cvt_pk_bf16_f32 v1, v20, v21
	v_mfma_f32_16x16x32_bf16 v[20:23], v[92:95], v[8:11], 0
	v_mfma_f32_16x16x32_bf16 v[8:11], v[104:107], v[8:11], 0
	v_mfma_f32_16x16x32_bf16 v[20:23], v[108:111], v[12:15], v[20:23]
	v_mfma_f32_16x16x32_bf16 v[8:11], v[120:123], v[12:15], v[8:11]
	v_mfma_f32_16x16x32_bf16 v[12:15], v[124:127], v[16:19], v[20:23]
	v_mfma_f32_16x16x32_bf16 v[20:23], v[128:131], v[16:19], v[24:27]
	v_mfma_f32_16x16x32_bf16 v[24:27], v[132:135], v[16:19], v[28:31]
	v_mfma_f32_16x16x32_bf16 v[8:11], v[136:139], v[16:19], v[8:11]
	v_mfma_f32_16x16x32_bf16 v[12:15], v[140:143], v[4:7], v[12:15]
	v_mfma_f32_16x16x32_bf16 v[16:19], v[144:147], v[4:7], v[20:23]
	v_mfma_f32_16x16x32_bf16 v[20:23], v[148:151], v[4:7], v[24:27]
	v_mfma_f32_16x16x32_bf16 v[4:7], v[152:155], v[4:7], v[8:11]
	v_mfma_f32_16x16x32_bf16 v[8:11], v[84:87], v[0:3], v[12:15]
	v_mfma_f32_16x16x32_bf16 v[12:15], v[156:159], v[0:3], v[16:19]
	v_mfma_f32_16x16x32_bf16 v[16:19], v[88:91], v[0:3], v[20:23]
	s_nop 5
	v_cvt_pk_bf16_f32 v8, v8, v9
	v_cvt_pk_bf16_f32 v9, v10, v11
	v_mfma_f32_16x16x32_bf16 v[4:7], v[160:163], v[0:3], v[4:7]
	v_lshl_add_u64 v[0:1], v[180:181], 0, s[34:35]
	global_store_dwordx2 v[0:1], v[8:9], off
	v_cvt_pk_bf16_f32 v8, v12, v13
	v_cvt_pk_bf16_f32 v9, v14, v15
	global_store_dwordx2 v[0:1], v[8:9], off offset:32
	v_cvt_pk_bf16_f32 v8, v16, v17
	v_cvt_pk_bf16_f32 v9, v18, v19
	s_nop 0
	v_cvt_pk_bf16_f32 v4, v4, v5
	v_cvt_pk_bf16_f32 v5, v6, v7
	global_store_dwordx2 v[0:1], v[8:9], off offset:64
	global_store_dwordx2 v[0:1], v[4:5], off offset:96
	s_cbranch_scc0 .LBB0_536

; #define PG8_ST16(rs, b0, p, v) __builtin_amdgcn_raw_buffer_store_b128(v, rs, (int)((const char*)(p) - (const char*)(b0)), 0, 16)
; __device__ __forceinline__ unsigned cvt_pk_bf16(float lo, float hi) { unsigned r; asm volatile("v_cvt_pk_bf16_f32 %0, %1, %2" : "=v"(r) : "v"(lo), "v"(hi)); return r; }
;     __device__ __forceinline__ void operator()(const f32x4 (&acc)[2][2][4][2], const Unit& u, int wr, int wc, int fr, int fq) const {
;     ...
;             for (int m = 0; m < 4; ++m) { const size_t off = (size_t)(row0 + ai * HALF + m * 16) * ldc + col0;
; #pragma unroll
;                 for (int bj = 0; bj < 2; ++bj) {
;                     if (BASE_F32) { b0[m][bj] = *(const f32x4*)((const float*)base + off + bj * HALF); b1[m][bj] = *(const f32x4*)((const float*)base + off + bj * HALF + 4); }
;                     else { const u32x4 q = *(const u32x4*)((const bf16_t*)base + off + bj * HALF);
;                         b0[m][bj] = (f32x4){__uint_as_float(q.x << 16), __uint_as_float(q.x & 0xffff0000u), __uint_as_float(q.y << 16), __uint_as_float(q.y & 0xffff0000u)};
;                         b1[m][bj] = (f32x4){__uint_as_float(q.z << 16), __uint_as_float(q.z & 0xffff0000u), __uint_as_float(q.w << 16), __uint_as_float(q.w & 0xffff0000u)}; } } }
;             asm volatile("" ::: "memory");
; #pragma unroll
;             for (int m = 0; m < 4; ++m) { const size_t off = (size_t)(row0 + ai * HALF + m * 16) * ldc + col0; float ssq = 0.f;
; #pragma unroll
;                 for (int bj = 0; bj < 2; ++bj) {
;                     const f32x4 o0 = b0[m][bj] + acc[ai][bj][m][0] * sc, o1 = b1[m][bj] + acc[ai][bj][m][1] * sc;
;                     ssq += ((o0[0] * o0[0] + o0[1] * o0[1]) + (o0[2] * o0[2] + o0[3] * o0[3])) + ((o1[0] * o1[0] + o1[1] * o1[1]) + (o1[2] * o1[2] + o1[3] * o1[3]));
;                     u32x4 w; w.x = cvt_pk_bf16(o0[0], o0[1]); w.y = cvt_pk_bf16(o0[2], o0[3]); w.z = cvt_pk_bf16(o1[0], o1[1]); w.w = cvt_pk_bf16(o1[2], o1[3]);
;                     PG8_ST16(rs_, out, out + off + bj * HALF, w); }
;                 ssq += __shfl_xor(ssq, 16); ssq += __shfl_xor(ssq, 32);
;                 if (fq == 0) rowss[(size_t)(row0 + ai * HALF + m * 16) * 32 + 4 * u.pn + wc] = ssq; }
.LBB0_822:
	v_lshl_or_b32 v36, s70, 8, v188
	v_lshl_add_u32 v38, s71, 8, v186
	v_ashrrev_i32_e32 v37, 31, v36
	v_lshlrev_b64 v[192:193], 1, v[36:37]
	v_ashrrev_i32_e32 v39, 31, v38
	v_lshl_add_u64 v[40:41], s[20:21], 0, v[192:193]
	v_lshlrev_b64 v[190:191], 12, v[38:39]
	v_lshl_add_u64 v[4:5], v[40:41], 0, v[190:191]
	global_load_dwordx4 v[60:63], v[4:5], off
	global_load_dwordx4 v[76:79], v[4:5], off offset:256
	v_or_b32_e32 v54, 16, v38
	v_or_b32_e32 v52, 32, v38
	v_or_b32_e32 v42, 48, v38
	v_ashrrev_i32_e32 v55, 31, v54
	v_ashrrev_i32_e32 v53, 31, v52
	v_ashrrev_i32_e32 v43, 31, v42
	v_lshlrev_b64 v[4:5], 12, v[54:55]
	v_lshlrev_b64 v[6:7], 12, v[52:53]
	v_lshlrev_b64 v[8:9], 12, v[42:43]
	v_lshl_add_u64 v[4:5], v[40:41], 0, v[4:5]
	v_lshl_add_u64 v[6:7], v[40:41], 0, v[6:7]
	v_lshl_add_u64 v[194:195], v[40:41], 0, v[8:9]
	global_load_dwordx4 v[24:27], v[4:5], off
	global_load_dwordx4 v[20:23], v[4:5], off offset:256
	global_load_dwordx4 v[16:19], v[6:7], off
	global_load_dwordx4 v[12:15], v[6:7], off offset:256
	global_load_dwordx4 v[8:11], v[194:195], off
	s_nop 0
	global_load_dwordx4 v[4:7], v[194:195], off offset:256
	v_and_b32_e32 v195, 64, v215
	v_xor_b32_e32 v194, 16, v215
	v_add_u32_e32 v195, 64, v195
	v_xor_b32_e32 v196, 32, v215
	v_cmp_lt_i32_e32 vcc, v194, v195
	s_lshl_b32 s42, s70, 2
	s_ashr_i32 s43, s42, 31
	v_cndmask_b32_e32 v197, v215, v194, vcc
	v_cmp_lt_i32_e32 vcc, v196, v195
	v_lshl_add_u64 v[194:195], s[20:21], 0, v[190:191]
	v_lshlrev_b32_e32 v190, 2, v197
	v_cndmask_b32_e32 v202, v215, v196, vcc
	v_lshl_add_u64 v[192:193], v[194:195], 0, v[192:193]
	s_waitcnt vmcnt(0)
	v_lshlrev_b32_e32 v194, 16, v60
	v_and_b32_e32 v195, 0xffff0000, v60
	v_lshlrev_b32_e32 v60, 16, v61
	v_and_b32_e32 v61, 0xffff0000, v61
	v_lshlrev_b32_e32 v196, 16, v62
	v_and_b32_e32 v197, 0xffff0000, v62
	v_lshlrev_b32_e32 v62, 16, v63
	v_and_b32_e32 v63, 0xffff0000, v63
	v_lshlrev_b32_e32 v198, 16, v76
	v_and_b32_e32 v199, 0xffff0000, v76
	v_lshlrev_b32_e32 v76, 16, v77
	v_and_b32_e32 v77, 0xffff0000, v77
	v_lshlrev_b32_e32 v200, 16, v78
	v_and_b32_e32 v201, 0xffff0000, v78
	v_lshlrev_b32_e32 v78, 16, v79
	v_and_b32_e32 v79, 0xffff0000, v79
	v_pk_add_f32 v[162:163], v[162:163], v[60:61]
	v_pk_add_f32 v[160:161], v[160:161], v[194:195]
	v_pk_add_f32 v[174:175], v[174:175], v[62:63]
	v_pk_add_f32 v[62:63], v[176:177], v[196:197]
	v_pk_add_f32 v[176:177], v[178:179], v[76:77]
	v_pk_add_f32 v[76:77], v[180:181], v[198:199]
	v_pk_add_f32 v[178:179], v[182:183], v[78:79]
	v_pk_add_f32 v[78:79], v[184:185], v[200:201]
	v_mul_f32_e32 v180, v161, v161
	v_mul_f32_e32 v181, v163, v163
	v_mul_f32_e32 v182, v63, v63
	v_mul_f32_e32 v183, v175, v175
	v_cvt_pk_bf16_f32 v60, v160, v161
	v_cvt_pk_bf16_f32 v61, v162, v163
	v_mul_f32_e32 v161, v77, v77
	v_mul_f32_e32 v163, v177, v177
	v_mul_f32_e32 v184, v79, v79
	v_mul_f32_e32 v185, v179, v179
	v_fmac_f32_e32 v180, v160, v160
	v_fmac_f32_e32 v181, v162, v162
	v_fmac_f32_e32 v182, v62, v62
	v_fmac_f32_e32 v183, v174, v174
	v_fmac_f32_e32 v161, v76, v76
	v_fmac_f32_e32 v163, v176, v176
	v_fmac_f32_e32 v184, v78, v78
	v_fmac_f32_e32 v185, v178, v178
	v_add_f32_e32 v160, v180, v181
	v_add_f32_e32 v162, v182, v183
	v_add_f32_e32 v161, v161, v163
	v_add_f32_e32 v163, v184, v185
	v_add_f32_e32 v160, v160, v162
	v_add_f32_e32 v161, v161, v163
	v_add_f32_e32 v160, v160, v161
	ds_bpermute_b32 v161, v190, v160
	v_cvt_pk_bf16_f32 v62, v62, v63
	v_cvt_pk_bf16_f32 v63, v174, v175
	global_store_dwordx4 v[192:193], v[60:63], off
	v_cvt_pk_bf16_f32 v76, v76, v77
	v_cvt_pk_bf16_f32 v77, v176, v177
	v_cvt_pk_bf16_f32 v78, v78, v79
	v_cvt_pk_bf16_f32 v79, v178, v179
	global_store_dwordx4 v[192:193], v[76:79], off offset:256
	s_waitcnt lgkmcnt(0)
	v_add_f32_e32 v60, v160, v161
	v_lshlrev_b32_e32 v160, 2, v202
	v_mov_b32_e32 v61, v60
	s_nop 1
	v_permlane32_swap_b32_e32 v61, v60
	s_and_saveexec_b64 s[44:45], s[36:37]
	s_cbranch_execz .LBB0_824
	v_lshlrev_b64 v[62:63], 7, v[38:39]
	v_lshl_add_u64 v[62:63], s[22:23], 0, v[62:63]
	v_lshl_add_u64 v[62:63], s[42:43], 2, v[62:63]
	s_lshl_b32 s46, s62, 2
	s_mov_b32 s47, s31
	v_lshl_add_u64 v[62:63], v[62:63], 0, s[46:47]
	s_waitcnt lgkmcnt(0)
	v_add_f32_e32 v39, v60, v61
	global_store_dword v[62:63], v39, off
.LBB0_824:
	s_or_b64 exec, exec, s[44:45]
	v_lshlrev_b32_e32 v62, 16, v24
	v_and_b32_e32 v63, 0xffff0000, v24
	v_lshlrev_b32_e32 v24, 16, v25
	v_and_b32_e32 v25, 0xffff0000, v25
	v_lshlrev_b32_e32 v78, 16, v20
	v_and_b32_e32 v79, 0xffff0000, v20
	v_lshlrev_b32_e32 v162, 16, v21
	v_and_b32_e32 v163, 0xffff0000, v21
	v_lshlrev_b32_e32 v174, 16, v22
	v_and_b32_e32 v175, 0xffff0000, v22
	v_lshlrev_b32_e32 v176, 16, v23
	v_and_b32_e32 v177, 0xffff0000, v23
	v_pk_add_f32 v[22:23], v[158:159], v[24:25]
	v_pk_add_f32 v[20:21], v[156:157], v[62:63]
	v_lshlrev_b32_e32 v76, 16, v26
	v_and_b32_e32 v77, 0xffff0000, v26
	v_lshlrev_b32_e32 v26, 16, v27
	v_and_b32_e32 v27, 0xffff0000, v27
	v_mul_f32_e32 v39, v21, v21
	v_mul_f32_e32 v62, v23, v23
	v_pk_add_f32 v[24:25], v[154:155], v[26:27]
	v_pk_add_f32 v[26:27], v[152:153], v[76:77]
	v_fmac_f32_e32 v39, v20, v20
	v_fmac_f32_e32 v62, v22, v22
	v_add_f32_e32 v39, v39, v62
	v_mul_f32_e32 v62, v27, v27
	v_mul_f32_e32 v63, v25, v25
	v_fmac_f32_e32 v62, v26, v26
	v_fmac_f32_e32 v63, v24, v24
	v_cvt_pk_bf16_f32 v20, v20, v21
	v_cvt_pk_bf16_f32 v21, v22, v23
	v_cvt_pk_bf16_f32 v22, v26, v27
	v_cvt_pk_bf16_f32 v23, v24, v25
	v_pk_add_f32 v[24:25], v[150:151], v[162:163]
	v_pk_add_f32 v[26:27], v[148:149], v[78:79]
	v_add_f32_e32 v62, v62, v63
	v_mul_f32_e32 v78, v27, v27
	v_mul_f32_e32 v79, v25, v25
	v_add_f32_e32 v39, v39, v62
	v_pk_add_f32 v[62:63], v[146:147], v[176:177]
	v_pk_add_f32 v[76:77], v[144:145], v[174:175]
	v_fmac_f32_e32 v78, v26, v26
	v_fmac_f32_e32 v79, v24, v24
	v_add_f32_e32 v78, v78, v79
	v_mul_f32_e32 v79, v77, v77
	v_mul_f32_e32 v144, v63, v63
	v_fmac_f32_e32 v79, v76, v76
	v_fmac_f32_e32 v144, v62, v62
	v_add_f32_e32 v79, v79, v144
	v_add_f32_e32 v78, v78, v79
	v_add_f32_e32 v39, v39, v78
	v_mov_b32_e32 v78, v39
	s_nop 1
	v_permlane16_swap_b32_e32 v78, v39
	s_waitcnt lgkmcnt(1)
	v_lshlrev_b64 v[60:61], 11, v[54:55]
	v_lshl_add_u64 v[60:61], v[60:61], 1, s[20:21]
	v_lshl_add_u64 v[60:61], v[36:37], 1, v[60:61]
	global_store_dwordx4 v[60:61], v[20:23], off
	s_waitcnt lgkmcnt(0)
	s_nop 0
	v_add_f32_e32 v20, v39, v78
	v_mov_b32_e32 v21, v20
	s_nop 1
	v_permlane32_swap_b32_e32 v21, v20
	v_cvt_pk_bf16_f32 v22, v26, v27
	v_cvt_pk_bf16_f32 v23, v24, v25
	v_cvt_pk_bf16_f32 v24, v76, v77
	v_cvt_pk_bf16_f32 v25, v62, v63
	global_store_dwordx4 v[60:61], v[22:25], off offset:256
	s_and_saveexec_b64 s[44:45], s[36:37]
	s_cbranch_execz .LBB0_826
	v_lshlrev_b64 v[22:23], 7, v[54:55]
	v_lshl_add_u64 v[22:23], s[22:23], 0, v[22:23]
	v_lshl_add_u64 v[22:23], s[42:43], 2, v[22:23]
	s_lshl_b32 s46, s62, 2
	s_mov_b32 s47, s31
	v_lshl_add_u64 v[22:23], v[22:23], 0, s[46:47]
	s_waitcnt lgkmcnt(0)
	v_add_f32_e32 v20, v20, v21
	global_store_dword v[22:23], v20, off
; #define PG8_ST16(rs, b0, p, v) __builtin_amdgcn_raw_buffer_store_b128(v, rs, (int)((const char*)(p) - (const char*)(b0)), 0, 16)
; __device__ __forceinline__ unsigned cvt_pk_bf16(float lo, float hi) { unsigned r; asm volatile("v_cvt_pk_bf16_f32 %0, %1, %2" : "=v"(r) : "v"(lo), "v"(hi)); return r; }
;     __device__ __forceinline__ void operator()(const f32x4 (&acc)[2][2][4][2], const Unit& u, int wr, int wc, int fr, int fq) const {
;     ...
;             for (int m = 0; m < 4; ++m) { const size_t off = (size_t)(row0 + ai * HALF + m * 16) * ldc + col0;
; #pragma unroll
;                 for (int bj = 0; bj < 2; ++bj) {
;                     if (BASE_F32) { b0[m][bj] = *(const f32x4*)((const float*)base + off + bj * HALF); b1[m][bj] = *(const f32x4*)((const float*)base + off + bj * HALF + 4); }
;                     else { const u32x4 q = *(const u32x4*)((const bf16_t*)base + off + bj * HALF);
;                         b0[m][bj] = (f32x4){__uint_as_float(q.x << 16), __uint_as_float(q.x & 0xffff0000u), __uint_as_float(q.y << 16), __uint_as_float(q.y & 0xffff0000u)};
;                         b1[m][bj] = (f32x4){__uint_as_float(q.z << 16), __uint_as_float(q.z & 0xffff0000u), __uint_as_float(q.w << 16), __uint_as_float(q.w & 0xffff0000u)}; } } }
;             asm volatile("" ::: "memory");
; #pragma unroll
;             for (int m = 0; m < 4; ++m) { const size_t off = (size_t)(row0 + ai * HALF + m * 16) * ldc + col0; float ssq = 0.f;
; #pragma unroll
;                 for (int bj = 0; bj < 2; ++bj) {
;                     const f32x4 o0 = b0[m][bj] + acc[ai][bj][m][0] * sc, o1 = b1[m][bj] + acc[ai][bj][m][1] * sc;
;                     ssq += ((o0[0] * o0[0] + o0[1] * o0[1]) + (o0[2] * o0[2] + o0[3] * o0[3])) + ((o1[0] * o1[0] + o1[1] * o1[1]) + (o1[2] * o1[2] + o1[3] * o1[3]));
;                     u32x4 w; w.x = cvt_pk_bf16(o0[0], o0[1]); w.y = cvt_pk_bf16(o0[2], o0[3]); w.z = cvt_pk_bf16(o1[0], o1[1]); w.w = cvt_pk_bf16(o1[2], o1[3]);
;                     PG8_ST16(rs_, out, out + off + bj * HALF, w); }
;                 ssq += __shfl_xor(ssq, 16); ssq += __shfl_xor(ssq, 32);
;                 if (fq == 0) rowss[(size_t)(row0 + ai * HALF + m * 16) * 32 + 4 * u.pn + wc] = ssq; }
.LBB0_826:
	s_or_b64 exec, exec, s[44:45]
	v_lshlrev_b32_e32 v22, 16, v16
	v_and_b32_e32 v23, 0xffff0000, v16
	v_lshlrev_b32_e32 v16, 16, v17
	v_and_b32_e32 v17, 0xffff0000, v17
	v_lshlrev_b32_e32 v26, 16, v12
	v_and_b32_e32 v27, 0xffff0000, v12
	v_lshlrev_b32_e32 v54, 16, v13
	v_and_b32_e32 v55, 0xffff0000, v13
	v_lshlrev_b32_e32 v60, 16, v14
	v_and_b32_e32 v61, 0xffff0000, v14
	v_lshlrev_b32_e32 v62, 16, v15
	v_and_b32_e32 v63, 0xffff0000, v15
	v_pk_add_f32 v[14:15], v[142:143], v[16:17]
	v_pk_add_f32 v[12:13], v[140:141], v[22:23]
	v_lshlrev_b32_e32 v24, 16, v18
	v_and_b32_e32 v25, 0xffff0000, v18
	v_lshlrev_b32_e32 v18, 16, v19
	v_and_b32_e32 v19, 0xffff0000, v19
	v_mul_f32_e32 v22, v13, v13
	v_mul_f32_e32 v23, v15, v15
	v_pk_add_f32 v[16:17], v[138:139], v[18:19]
	v_pk_add_f32 v[18:19], v[136:137], v[24:25]
	v_fmac_f32_e32 v22, v12, v12
	v_fmac_f32_e32 v23, v14, v14
	v_add_f32_e32 v22, v22, v23
	v_mul_f32_e32 v23, v19, v19
	v_mul_f32_e32 v24, v17, v17
	v_fmac_f32_e32 v23, v18, v18
	v_fmac_f32_e32 v24, v16, v16
	v_cvt_pk_bf16_f32 v12, v12, v13
	v_cvt_pk_bf16_f32 v13, v14, v15
	v_cvt_pk_bf16_f32 v14, v18, v19
	v_cvt_pk_bf16_f32 v15, v16, v17
	v_pk_add_f32 v[16:17], v[134:135], v[54:55]
	v_pk_add_f32 v[18:19], v[132:133], v[26:27]
	v_add_f32_e32 v23, v23, v24
	v_mul_f32_e32 v26, v19, v19
	v_mul_f32_e32 v27, v17, v17
	v_add_f32_e32 v39, v22, v23
	v_pk_add_f32 v[22:23], v[130:131], v[62:63]
	v_pk_add_f32 v[24:25], v[128:129], v[60:61]
	v_fmac_f32_e32 v26, v18, v18
	v_fmac_f32_e32 v27, v16, v16
	v_add_f32_e32 v26, v26, v27
	v_mul_f32_e32 v27, v25, v25
	v_mul_f32_e32 v54, v23, v23
	v_fmac_f32_e32 v27, v24, v24
	v_fmac_f32_e32 v54, v22, v22
	v_add_f32_e32 v27, v27, v54
	v_add_f32_e32 v26, v26, v27
	v_add_f32_e32 v26, v39, v26
	v_mov_b32_e32 v27, v26
	s_nop 1
	v_permlane16_swap_b32_e32 v27, v26
	s_waitcnt lgkmcnt(1)
	v_lshlrev_b64 v[20:21], 11, v[52:53]
	v_lshl_add_u64 v[20:21], v[20:21], 1, s[20:21]
	v_lshl_add_u64 v[20:21], v[36:37], 1, v[20:21]
	global_store_dwordx4 v[20:21], v[12:15], off
	s_waitcnt lgkmcnt(0)
	s_nop 0
	v_add_f32_e32 v12, v26, v27
	v_mov_b32_e32 v13, v12
	s_nop 1
	v_permlane32_swap_b32_e32 v13, v12
	v_cvt_pk_bf16_f32 v14, v18, v19
	v_cvt_pk_bf16_f32 v15, v16, v17
	v_cvt_pk_bf16_f32 v16, v24, v25
	v_cvt_pk_bf16_f32 v17, v22, v23
	global_store_dwordx4 v[20:21], v[14:17], off offset:256
	s_and_saveexec_b64 s[44:45], s[36:37]
	s_cbranch_execz .LBB0_828
	v_lshlrev_b64 v[14:15], 7, v[52:53]
	v_lshl_add_u64 v[14:15], s[22:23], 0, v[14:15]
	v_lshl_add_u64 v[14:15], s[42:43], 2, v[14:15]
	s_lshl_b32 s46, s62, 2
	s_mov_b32 s47, s31
	v_lshl_add_u64 v[14:15], v[14:15], 0, s[46:47]
	s_waitcnt lgkmcnt(0)
	v_add_f32_e32 v12, v12, v13
	global_store_dword v[14:15], v12, off
.LBB0_828:
	s_or_b64 exec, exec, s[44:45]
	v_lshlrev_b32_e32 v14, 16, v8
	v_and_b32_e32 v15, 0xffff0000, v8
	v_lshlrev_b32_e32 v8, 16, v9
	v_and_b32_e32 v9, 0xffff0000, v9
	v_lshlrev_b32_e32 v18, 16, v4
	v_and_b32_e32 v19, 0xffff0000, v4
	v_lshlrev_b32_e32 v20, 16, v5
	v_and_b32_e32 v21, 0xffff0000, v5
	v_lshlrev_b32_e32 v22, 16, v6
	v_and_b32_e32 v23, 0xffff0000, v6
	v_lshlrev_b32_e32 v24, 16, v7
	v_and_b32_e32 v25, 0xffff0000, v7
	v_pk_add_f32 v[6:7], v[126:127], v[8:9]
	v_pk_add_f32 v[4:5], v[124:125], v[14:15]
	v_lshlrev_b32_e32 v16, 16, v10
	v_and_b32_e32 v17, 0xffff0000, v10
	v_lshlrev_b32_e32 v10, 16, v11
	v_and_b32_e32 v11, 0xffff0000, v11
	v_mul_f32_e32 v14, v5, v5
	v_mul_f32_e32 v15, v7, v7
	v_pk_add_f32 v[8:9], v[122:123], v[10:11]
	v_pk_add_f32 v[10:11], v[120:121], v[16:17]
	v_fmac_f32_e32 v14, v4, v4
	v_fmac_f32_e32 v15, v6, v6
	v_add_f32_e32 v14, v14, v15
	v_mul_f32_e32 v15, v11, v11
	v_mul_f32_e32 v16, v9, v9
	v_fmac_f32_e32 v15, v10, v10
	v_fmac_f32_e32 v16, v8, v8
	v_cvt_pk_bf16_f32 v4, v4, v5
	v_cvt_pk_bf16_f32 v5, v6, v7
	v_cvt_pk_bf16_f32 v6, v10, v11
	v_cvt_pk_bf16_f32 v7, v8, v9
	v_pk_add_f32 v[8:9], v[118:119], v[20:21]
	v_pk_add_f32 v[10:11], v[116:117], v[18:19]
	v_add_f32_e32 v15, v15, v16
	v_mul_f32_e32 v18, v11, v11
	v_mul_f32_e32 v19, v9, v9
	v_add_f32_e32 v26, v14, v15
	v_pk_add_f32 v[14:15], v[114:115], v[24:25]
	v_pk_add_f32 v[16:17], v[112:113], v[22:23]
	v_fmac_f32_e32 v18, v10, v10
	v_fmac_f32_e32 v19, v8, v8
	v_add_f32_e32 v18, v18, v19
	v_mul_f32_e32 v19, v17, v17
	v_mul_f32_e32 v20, v15, v15
	v_fmac_f32_e32 v19, v16, v16
	v_fmac_f32_e32 v20, v14, v14
	v_add_f32_e32 v19, v19, v20
	v_add_f32_e32 v18, v18, v19
	v_add_f32_e32 v18, v26, v18
	v_mov_b32_e32 v19, v18
	s_nop 1
	v_permlane16_swap_b32_e32 v19, v18
	s_waitcnt lgkmcnt(1)
	v_lshlrev_b64 v[12:13], 11, v[42:43]
	v_lshl_add_u64 v[12:13], v[12:13], 1, s[20:21]
	v_lshl_add_u64 v[12:13], v[36:37], 1, v[12:13]
	global_store_dwordx4 v[12:13], v[4:7], off
	s_waitcnt lgkmcnt(0)
	s_nop 0
	v_add_f32_e32 v4, v18, v19
	v_mov_b32_e32 v5, v4
	s_nop 1
	v_permlane32_swap_b32_e32 v5, v4
	v_cvt_pk_bf16_f32 v6, v10, v11
	v_cvt_pk_bf16_f32 v7, v8, v9
	v_cvt_pk_bf16_f32 v8, v16, v17
	v_cvt_pk_bf16_f32 v9, v14, v15
	global_store_dwordx4 v[12:13], v[6:9], off offset:256
	s_and_saveexec_b64 s[44:45], s[36:37]
	s_cbranch_execz .LBB0_830
	v_lshlrev_b64 v[6:7], 7, v[42:43]
	v_lshl_add_u64 v[6:7], s[22:23], 0, v[6:7]
	v_lshl_add_u64 v[6:7], s[42:43], 2, v[6:7]
	s_lshl_b32 s46, s62, 2
	s_mov_b32 s47, s31
	v_lshl_add_u64 v[6:7], v[6:7], 0, s[46:47]
	s_waitcnt lgkmcnt(0)
	v_add_f32_e32 v4, v4, v5
	global_store_dword v[6:7], v4, off
; #define PG8_ST16(rs, b0, p, v) __builtin_amdgcn_raw_buffer_store_b128(v, rs, (int)((const char*)(p) - (const char*)(b0)), 0, 16)
; __device__ __forceinline__ unsigned cvt_pk_bf16(float lo, float hi) { unsigned r; asm volatile("v_cvt_pk_bf16_f32 %0, %1, %2" : "=v"(r) : "v"(lo), "v"(hi)); return r; }
;     __device__ __forceinline__ void operator()(const f32x4 (&acc)[2][2][4][2], const Unit& u, int wr, int wc, int fr, int fq) const {
;     ...
;             for (int m = 0; m < 4; ++m) { const size_t off = (size_t)(row0 + ai * HALF + m * 16) * ldc + col0;
; #pragma unroll
;                 for (int bj = 0; bj < 2; ++bj) {
;                     if (BASE_F32) { b0[m][bj] = *(const f32x4*)((const float*)base + off + bj * HALF); b1[m][bj] = *(const f32x4*)((const float*)base + off + bj * HALF + 4); }
;                     else { const u32x4 q = *(const u32x4*)((const bf16_t*)base + off + bj * HALF);
;                         b0[m][bj] = (f32x4){__uint_as_float(q.x << 16), __uint_as_float(q.x & 0xffff0000u), __uint_as_float(q.y << 16), __uint_as_float(q.y & 0xffff0000u)};
;                         b1[m][bj] = (f32x4){__uint_as_float(q.z << 16), __uint_as_float(q.z & 0xffff0000u), __uint_as_float(q.w << 16), __uint_as_float(q.w & 0xffff0000u)}; } } }
;             asm volatile("" ::: "memory");
; #pragma unroll
;             for (int m = 0; m < 4; ++m) { const size_t off = (size_t)(row0 + ai * HALF + m * 16) * ldc + col0; float ssq = 0.f;
; #pragma unroll
;                 for (int bj = 0; bj < 2; ++bj) {
;                     const f32x4 o0 = b0[m][bj] + acc[ai][bj][m][0] * sc, o1 = b1[m][bj] + acc[ai][bj][m][1] * sc;
;                     ssq += ((o0[0] * o0[0] + o0[1] * o0[1]) + (o0[2] * o0[2] + o0[3] * o0[3])) + ((o1[0] * o1[0] + o1[1] * o1[1]) + (o1[2] * o1[2] + o1[3] * o1[3]));
;                     u32x4 w; w.x = cvt_pk_bf16(o0[0], o0[1]); w.y = cvt_pk_bf16(o0[2], o0[3]); w.z = cvt_pk_bf16(o1[0], o1[1]); w.w = cvt_pk_bf16(o1[2], o1[3]);
;                     PG8_ST16(rs_, out, out + off + bj * HALF, w); }
;                 ssq += __shfl_xor(ssq, 16); ssq += __shfl_xor(ssq, 32);
;                 if (fq == 0) rowss[(size_t)(row0 + ai * HALF + m * 16) * 32 + 4 * u.pn + wc] = ssq; }
.LBB0_830:
	s_or_b64 exec, exec, s[44:45]
	v_add_u32_e32 v54, 0x80, v38
	v_ashrrev_i32_e32 v55, 31, v54
	v_lshlrev_b64 v[112:113], 12, v[54:55]
	v_lshl_add_u64 v[8:9], v[40:41], 0, v[112:113]
	s_waitcnt lgkmcnt(0)
	global_load_dwordx4 v[222:225], v[8:9], off
	global_load_dwordx4 v[218:221], v[8:9], off offset:256
	v_add_u32_e32 v52, 0x90, v38
	v_ashrrev_i32_e32 v53, 31, v52
	v_add_u32_e32 v42, 0xa0, v38
	v_ashrrev_i32_e32 v43, 31, v42
	v_add_u32_e32 v38, 0xb0, v38
	v_ashrrev_i32_e32 v39, 31, v38
	v_lshlrev_b64 v[4:5], 12, v[52:53]
	v_lshl_add_u64 v[4:5], v[40:41], 0, v[4:5]
	global_load_dwordx4 v[24:27], v[4:5], off
	global_load_dwordx4 v[20:23], v[4:5], off offset:256
	v_lshlrev_b64 v[4:5], 12, v[42:43]
	v_lshl_add_u64 v[4:5], v[40:41], 0, v[4:5]
	global_load_dwordx4 v[16:19], v[4:5], off
	global_load_dwordx4 v[12:15], v[4:5], off offset:256
	v_lshlrev_b64 v[4:5], 12, v[38:39]
	v_lshl_add_u64 v[4:5], v[40:41], 0, v[4:5]
	global_load_dwordx4 v[8:11], v[4:5], off
	s_nop 0
	global_load_dwordx4 v[4:7], v[4:5], off offset:256
	s_waitcnt vmcnt(6)
	v_lshlrev_b32_e32 v116, 16, v222
	v_and_b32_e32 v117, 0xffff0000, v222
	v_lshlrev_b32_e32 v120, 16, v223
	v_and_b32_e32 v121, 0xffff0000, v223
	v_lshlrev_b32_e32 v114, 16, v224
	v_and_b32_e32 v115, 0xffff0000, v224
	v_lshlrev_b32_e32 v118, 16, v225
	v_and_b32_e32 v119, 0xffff0000, v225
	v_pk_add_f32 v[108:109], v[108:109], v[116:117]
	v_lshlrev_b32_e32 v62, 16, v218
	v_and_b32_e32 v63, 0xffff0000, v218
	v_lshlrev_b32_e32 v78, 16, v219
	v_and_b32_e32 v79, 0xffff0000, v219
	v_lshlrev_b32_e32 v60, 16, v220
	v_and_b32_e32 v61, 0xffff0000, v220
	v_lshlrev_b32_e32 v76, 16, v221
	v_and_b32_e32 v77, 0xffff0000, v221
	v_pk_add_f32 v[40:41], v[110:111], v[120:121]
	v_pk_add_f32 v[78:79], v[102:103], v[78:79]
	v_pk_add_f32 v[62:63], v[100:101], v[62:63]
	v_pk_add_f32 v[110:111], v[106:107], v[118:119]
	v_pk_add_f32 v[106:107], v[104:105], v[114:115]
	v_mul_f32_e32 v104, v109, v109
	v_mul_f32_e32 v105, v41, v41
	v_pk_add_f32 v[96:97], v[96:97], v[60:61]
	v_mul_f32_e32 v60, v63, v63
	v_mul_f32_e32 v61, v79, v79
	v_fmac_f32_e32 v104, v108, v108
	v_fmac_f32_e32 v105, v40, v40
	v_pk_add_f32 v[76:77], v[98:99], v[76:77]
	v_fmac_f32_e32 v60, v62, v62
	v_fmac_f32_e32 v61, v78, v78
	v_add_f32_e32 v104, v104, v105
	v_mul_f32_e32 v105, v107, v107
	v_mul_f32_e32 v114, v111, v111
	v_add_f32_e32 v60, v60, v61
	v_mul_f32_e32 v61, v97, v97
	v_mul_f32_e32 v98, v77, v77
	v_fmac_f32_e32 v105, v106, v106
	v_fmac_f32_e32 v114, v110, v110
	v_fmac_f32_e32 v61, v96, v96
	v_fmac_f32_e32 v98, v76, v76
	v_add_f32_e32 v105, v105, v114
	v_add_f32_e32 v61, v61, v98
	v_add_f32_e32 v114, v104, v105
	v_cvt_pk_bf16_f32 v104, v108, v109
	v_cvt_pk_bf16_f32 v105, v40, v41
	v_lshl_add_u64 v[40:41], s[20:21], 0, v[112:113]
	v_add_f32_e32 v60, v60, v61
	v_lshl_add_u64 v[40:41], v[36:37], 1, v[40:41]
	v_add_f32_e32 v98, v114, v60
	v_cvt_pk_bf16_f32 v106, v106, v107
	v_cvt_pk_bf16_f32 v107, v110, v111
	global_store_dwordx4 v[40:41], v[104:107], off
	v_cvt_pk_bf16_f32 v60, v62, v63
	v_cvt_pk_bf16_f32 v61, v78, v79
	v_cvt_pk_bf16_f32 v62, v96, v97
	v_cvt_pk_bf16_f32 v63, v76, v77
	global_store_dwordx4 v[40:41], v[60:63], off offset:256
	ds_bpermute_b32 v40, v190, v98
	s_waitcnt lgkmcnt(0)
	v_add_f32_e32 v40, v98, v40
	v_mov_b32_e32 v41, v40
	s_nop 1
	v_permlane32_swap_b32_e32 v41, v40
	s_and_saveexec_b64 s[44:45], s[36:37]
	s_cbranch_execz .LBB0_832
	v_lshlrev_b64 v[54:55], 7, v[54:55]
	v_lshl_add_u64 v[54:55], s[22:23], 0, v[54:55]
	v_lshl_add_u64 v[54:55], s[42:43], 2, v[54:55]
	s_lshl_b32 s46, s62, 2
	s_mov_b32 s47, s31
	v_lshl_add_u64 v[54:55], v[54:55], 0, s[46:47]
	s_waitcnt lgkmcnt(0)
	v_add_f32_e32 v40, v40, v41
	global_store_dword v[54:55], v40, off
.LBB0_832:
	s_or_b64 exec, exec, s[44:45]
	s_waitcnt vmcnt(7)
	v_lshlrev_b32_e32 v54, 16, v24
	v_and_b32_e32 v55, 0xffff0000, v24
	v_lshlrev_b32_e32 v24, 16, v25
	v_and_b32_e32 v25, 0xffff0000, v25
	s_waitcnt vmcnt(6)
	v_lshlrev_b32_e32 v62, 16, v20
	v_and_b32_e32 v63, 0xffff0000, v20
	v_lshlrev_b32_e32 v76, 16, v21
	v_and_b32_e32 v77, 0xffff0000, v21
	v_lshlrev_b32_e32 v78, 16, v22
	v_and_b32_e32 v79, 0xffff0000, v22
	v_lshlrev_b32_e32 v96, 16, v23
	v_and_b32_e32 v97, 0xffff0000, v23
	v_pk_add_f32 v[22:23], v[94:95], v[24:25]
	v_pk_add_f32 v[20:21], v[92:93], v[54:55]
	v_lshlrev_b32_e32 v60, 16, v26
	v_and_b32_e32 v61, 0xffff0000, v26
	v_lshlrev_b32_e32 v26, 16, v27
	v_and_b32_e32 v27, 0xffff0000, v27
	v_mul_f32_e32 v54, v21, v21
	v_mul_f32_e32 v55, v23, v23
	v_pk_add_f32 v[24:25], v[90:91], v[26:27]
	v_pk_add_f32 v[26:27], v[88:89], v[60:61]
	v_fmac_f32_e32 v54, v20, v20
	v_fmac_f32_e32 v55, v22, v22
	v_add_f32_e32 v54, v54, v55
	v_mul_f32_e32 v55, v27, v27
	v_mul_f32_e32 v60, v25, v25
	v_fmac_f32_e32 v55, v26, v26
	v_fmac_f32_e32 v60, v24, v24
	v_cvt_pk_bf16_f32 v20, v20, v21
	v_cvt_pk_bf16_f32 v21, v22, v23
	v_cvt_pk_bf16_f32 v22, v26, v27
	v_cvt_pk_bf16_f32 v23, v24, v25
	v_pk_add_f32 v[24:25], v[86:87], v[76:77]
	v_pk_add_f32 v[26:27], v[84:85], v[62:63]
	v_add_f32_e32 v55, v55, v60
	v_mul_f32_e32 v62, v27, v27
	v_mul_f32_e32 v63, v25, v25
	v_add_f32_e32 v88, v54, v55
	v_pk_add_f32 v[54:55], v[82:83], v[96:97]
	v_pk_add_f32 v[60:61], v[80:81], v[78:79]
	v_fmac_f32_e32 v62, v26, v26
	v_fmac_f32_e32 v63, v24, v24
	v_add_f32_e32 v62, v62, v63
	v_mul_f32_e32 v63, v61, v61
	v_mul_f32_e32 v76, v55, v55
	v_fmac_f32_e32 v63, v60, v60
	v_fmac_f32_e32 v76, v54, v54
	v_add_f32_e32 v63, v63, v76
	v_add_f32_e32 v62, v62, v63
	v_add_f32_e32 v62, v88, v62
	ds_bpermute_b32 v63, v190, v62
	s_waitcnt lgkmcnt(1)
	v_lshlrev_b64 v[40:41], 11, v[52:53]
	v_lshl_add_u64 v[40:41], v[40:41], 1, s[20:21]
	v_lshl_add_u64 v[40:41], v[36:37], 1, v[40:41]
	global_store_dwordx4 v[40:41], v[20:23], off
	s_waitcnt lgkmcnt(0)
	s_nop 0
	v_add_f32_e32 v20, v62, v63
	v_mov_b32_e32 v21, v20
	s_nop 1
	v_permlane32_swap_b32_e32 v21, v20
	v_cvt_pk_bf16_f32 v22, v26, v27
	v_cvt_pk_bf16_f32 v23, v24, v25
	v_cvt_pk_bf16_f32 v24, v60, v61
	v_cvt_pk_bf16_f32 v25, v54, v55
	global_store_dwordx4 v[40:41], v[22:25], off offset:256
	s_and_saveexec_b64 s[44:45], s[36:37]
	s_cbranch_execz .LBB0_834
	v_lshlrev_b64 v[22:23], 7, v[52:53]
	v_lshl_add_u64 v[22:23], s[22:23], 0, v[22:23]
	v_lshl_add_u64 v[22:23], s[42:43], 2, v[22:23]
	s_lshl_b32 s46, s62, 2
	s_mov_b32 s47, s31
	v_lshl_add_u64 v[22:23], v[22:23], 0, s[46:47]
	s_waitcnt lgkmcnt(0)
	v_add_f32_e32 v20, v20, v21
	global_store_dword v[22:23], v20, off
; #define PG8_ST16(rs, b0, p, v) __builtin_amdgcn_raw_buffer_store_b128(v, rs, (int)((const char*)(p) - (const char*)(b0)), 0, 16)
; __device__ __forceinline__ unsigned cvt_pk_bf16(float lo, float hi) { unsigned r; asm volatile("v_cvt_pk_bf16_f32 %0, %1, %2" : "=v"(r) : "v"(lo), "v"(hi)); return r; }
;     __device__ __forceinline__ void operator()(const f32x4 (&acc)[2][2][4][2], const Unit& u, int wr, int wc, int fr, int fq) const {
;     ...
;             for (int m = 0; m < 4; ++m) { const size_t off = (size_t)(row0 + ai * HALF + m * 16) * ldc + col0;
; #pragma unroll
;                 for (int bj = 0; bj < 2; ++bj) {
;                     if (BASE_F32) { b0[m][bj] = *(const f32x4*)((const float*)base + off + bj * HALF); b1[m][bj] = *(const f32x4*)((const float*)base + off + bj * HALF + 4); }
;                     else { const u32x4 q = *(const u32x4*)((const bf16_t*)base + off + bj * HALF);
;                         b0[m][bj] = (f32x4){__uint_as_float(q.x << 16), __uint_as_float(q.x & 0xffff0000u), __uint_as_float(q.y << 16), __uint_as_float(q.y & 0xffff0000u)};
;                         b1[m][bj] = (f32x4){__uint_as_float(q.z << 16), __uint_as_float(q.z & 0xffff0000u), __uint_as_float(q.w << 16), __uint_as_float(q.w & 0xffff0000u)}; } } }
;             asm volatile("" ::: "memory");
; #pragma unroll
;             for (int m = 0; m < 4; ++m) { const size_t off = (size_t)(row0 + ai * HALF + m * 16) * ldc + col0; float ssq = 0.f;
; #pragma unroll
;                 for (int bj = 0; bj < 2; ++bj) {
;                     const f32x4 o0 = b0[m][bj] + acc[ai][bj][m][0] * sc, o1 = b1[m][bj] + acc[ai][bj][m][1] * sc;
;                     ssq += ((o0[0] * o0[0] + o0[1] * o0[1]) + (o0[2] * o0[2] + o0[3] * o0[3])) + ((o1[0] * o1[0] + o1[1] * o1[1]) + (o1[2] * o1[2] + o1[3] * o1[3]));
;                     u32x4 w; w.x = cvt_pk_bf16(o0[0], o0[1]); w.y = cvt_pk_bf16(o0[2], o0[3]); w.z = cvt_pk_bf16(o1[0], o1[1]); w.w = cvt_pk_bf16(o1[2], o1[3]);
;                     PG8_ST16(rs_, out, out + off + bj * HALF, w); }
;                 ssq += __shfl_xor(ssq, 16); ssq += __shfl_xor(ssq, 32);
;                 if (fq == 0) rowss[(size_t)(row0 + ai * HALF + m * 16) * 32 + 4 * u.pn + wc] = ssq; }
.LBB0_834:
	s_or_b64 exec, exec, s[44:45]
	s_waitcnt vmcnt(7)
	v_lshlrev_b32_e32 v22, 16, v16
	v_and_b32_e32 v23, 0xffff0000, v16
	v_lshlrev_b32_e32 v16, 16, v17
	v_and_b32_e32 v17, 0xffff0000, v17
	s_waitcnt vmcnt(6)
	v_lshlrev_b32_e32 v26, 16, v12
	v_and_b32_e32 v27, 0xffff0000, v12
	v_lshlrev_b32_e32 v40, 16, v13
	v_and_b32_e32 v41, 0xffff0000, v13
	v_lshlrev_b32_e32 v52, 16, v14
	v_and_b32_e32 v53, 0xffff0000, v14
	v_lshlrev_b32_e32 v54, 16, v15
	v_and_b32_e32 v55, 0xffff0000, v15
	v_pk_add_f32 v[14:15], v[74:75], v[16:17]
	v_pk_add_f32 v[12:13], v[72:73], v[22:23]
	v_lshlrev_b32_e32 v24, 16, v18
	v_and_b32_e32 v25, 0xffff0000, v18
	v_lshlrev_b32_e32 v18, 16, v19
	v_and_b32_e32 v19, 0xffff0000, v19
	v_mul_f32_e32 v22, v13, v13
	v_mul_f32_e32 v23, v15, v15
	v_pk_add_f32 v[16:17], v[70:71], v[18:19]
	v_pk_add_f32 v[18:19], v[68:69], v[24:25]
	v_fmac_f32_e32 v22, v12, v12
	v_fmac_f32_e32 v23, v14, v14
	v_add_f32_e32 v22, v22, v23
	v_mul_f32_e32 v23, v19, v19
	v_mul_f32_e32 v24, v17, v17
	v_fmac_f32_e32 v23, v18, v18
	v_fmac_f32_e32 v24, v16, v16
	v_cvt_pk_bf16_f32 v12, v12, v13
	v_cvt_pk_bf16_f32 v13, v14, v15
	v_cvt_pk_bf16_f32 v14, v18, v19
	v_cvt_pk_bf16_f32 v15, v16, v17
	v_pk_add_f32 v[16:17], v[66:67], v[40:41]
	v_pk_add_f32 v[18:19], v[64:65], v[26:27]
	v_add_f32_e32 v23, v23, v24
	v_mul_f32_e32 v26, v19, v19
	v_mul_f32_e32 v27, v17, v17
	v_add_f32_e32 v60, v22, v23
	v_pk_add_f32 v[22:23], v[58:59], v[54:55]
	v_pk_add_f32 v[24:25], v[56:57], v[52:53]
	v_fmac_f32_e32 v26, v18, v18
	v_fmac_f32_e32 v27, v16, v16
	v_add_f32_e32 v26, v26, v27
	v_mul_f32_e32 v27, v25, v25
	v_mul_f32_e32 v40, v23, v23
	v_fmac_f32_e32 v27, v24, v24
	v_fmac_f32_e32 v40, v22, v22
	v_add_f32_e32 v27, v27, v40
	v_add_f32_e32 v26, v26, v27
	v_add_f32_e32 v26, v60, v26
	ds_bpermute_b32 v27, v190, v26
	s_waitcnt lgkmcnt(1)
	v_lshlrev_b64 v[20:21], 11, v[42:43]
	v_lshl_add_u64 v[20:21], v[20:21], 1, s[20:21]
	v_lshl_add_u64 v[20:21], v[36:37], 1, v[20:21]
	global_store_dwordx4 v[20:21], v[12:15], off
	s_waitcnt lgkmcnt(0)
	s_nop 0
	v_add_f32_e32 v12, v26, v27
	v_mov_b32_e32 v13, v12
	s_nop 1
	v_permlane32_swap_b32_e32 v13, v12
	v_cvt_pk_bf16_f32 v14, v18, v19
	v_cvt_pk_bf16_f32 v15, v16, v17
	v_cvt_pk_bf16_f32 v16, v24, v25
	v_cvt_pk_bf16_f32 v17, v22, v23
	global_store_dwordx4 v[20:21], v[14:17], off offset:256
	s_and_saveexec_b64 s[44:45], s[36:37]
	s_cbranch_execz .LBB0_836
	v_lshlrev_b64 v[14:15], 7, v[42:43]
	v_lshl_add_u64 v[14:15], s[22:23], 0, v[14:15]
	v_lshl_add_u64 v[14:15], s[42:43], 2, v[14:15]
	s_lshl_b32 s46, s62, 2
	s_mov_b32 s47, s31
	v_lshl_add_u64 v[14:15], v[14:15], 0, s[46:47]
	s_waitcnt lgkmcnt(0)
	v_add_f32_e32 v12, v12, v13
	global_store_dword v[14:15], v12, off
.LBB0_836:
	s_or_b64 exec, exec, s[44:45]
	s_waitcnt vmcnt(7)
	v_lshlrev_b32_e32 v14, 16, v8
	v_and_b32_e32 v15, 0xffff0000, v8
	v_lshlrev_b32_e32 v8, 16, v9
	v_and_b32_e32 v9, 0xffff0000, v9
	s_waitcnt vmcnt(6)
	v_lshlrev_b32_e32 v18, 16, v4
	v_and_b32_e32 v19, 0xffff0000, v4
	v_lshlrev_b32_e32 v20, 16, v5
	v_and_b32_e32 v21, 0xffff0000, v5
	v_lshlrev_b32_e32 v22, 16, v6
	v_and_b32_e32 v23, 0xffff0000, v6
	v_lshlrev_b32_e32 v24, 16, v7
	v_and_b32_e32 v25, 0xffff0000, v7
	v_pk_add_f32 v[6:7], v[50:51], v[8:9]
	v_pk_add_f32 v[4:5], v[48:49], v[14:15]
	v_lshlrev_b32_e32 v16, 16, v10
	v_and_b32_e32 v17, 0xffff0000, v10
	v_lshlrev_b32_e32 v10, 16, v11
	v_and_b32_e32 v11, 0xffff0000, v11
	v_mul_f32_e32 v14, v5, v5
	v_mul_f32_e32 v15, v7, v7
	v_pk_add_f32 v[8:9], v[46:47], v[10:11]
	v_pk_add_f32 v[10:11], v[44:45], v[16:17]
	v_fmac_f32_e32 v14, v4, v4
	v_fmac_f32_e32 v15, v6, v6
	v_add_f32_e32 v14, v14, v15
	v_mul_f32_e32 v15, v11, v11
	v_mul_f32_e32 v16, v9, v9
	v_fmac_f32_e32 v15, v10, v10
	v_fmac_f32_e32 v16, v8, v8
	v_cvt_pk_bf16_f32 v4, v4, v5
	v_cvt_pk_bf16_f32 v5, v6, v7
	v_cvt_pk_bf16_f32 v6, v10, v11
	v_cvt_pk_bf16_f32 v7, v8, v9
	v_pk_add_f32 v[8:9], v[34:35], v[20:21]
	v_pk_add_f32 v[10:11], v[32:33], v[18:19]
	v_add_f32_e32 v15, v15, v16
	v_mul_f32_e32 v18, v11, v11
	v_mul_f32_e32 v19, v9, v9
	v_add_f32_e32 v26, v14, v15
	v_pk_add_f32 v[14:15], v[30:31], v[24:25]
	v_pk_add_f32 v[16:17], v[28:29], v[22:23]
	v_fmac_f32_e32 v18, v10, v10
	v_fmac_f32_e32 v19, v8, v8
	v_add_f32_e32 v18, v18, v19
	v_mul_f32_e32 v19, v17, v17
	v_mul_f32_e32 v20, v15, v15
	v_fmac_f32_e32 v19, v16, v16
	v_fmac_f32_e32 v20, v14, v14
	v_add_f32_e32 v19, v19, v20
	v_add_f32_e32 v18, v18, v19
	v_add_f32_e32 v18, v26, v18
	v_mov_b32_e32 v19, v18
	s_nop 1
	v_permlane16_swap_b32_e32 v19, v18
	s_waitcnt lgkmcnt(1)
	v_lshlrev_b64 v[12:13], 11, v[38:39]
	v_lshl_add_u64 v[12:13], v[12:13], 1, s[20:21]
	v_lshl_add_u64 v[12:13], v[36:37], 1, v[12:13]
	global_store_dwordx4 v[12:13], v[4:7], off
	s_waitcnt lgkmcnt(0)
	s_nop 0
	v_add_f32_e32 v4, v18, v19
	v_mov_b32_e32 v5, v4
	s_nop 1
	v_permlane32_swap_b32_e32 v5, v4
	v_cvt_pk_bf16_f32 v6, v10, v11
	v_cvt_pk_bf16_f32 v7, v8, v9
	v_cvt_pk_bf16_f32 v8, v16, v17
	v_cvt_pk_bf16_f32 v9, v14, v15
	global_store_dwordx4 v[12:13], v[6:9], off offset:256
	s_and_saveexec_b64 s[44:45], s[36:37]
	s_cbranch_execz .LBB0_838
	v_lshlrev_b64 v[6:7], 7, v[38:39]
	v_lshl_add_u64 v[6:7], s[22:23], 0, v[6:7]
	v_lshl_add_u64 v[6:7], s[42:43], 2, v[6:7]
	s_lshl_b32 s42, s62, 2
	s_mov_b32 s43, s31
	v_lshl_add_u64 v[6:7], v[6:7], 0, s[42:43]
	s_waitcnt lgkmcnt(0)
	v_add_f32_e32 v4, v4, v5
	global_store_dword v[6:7], v4, off

; #define PG8_ST16(rs, b0, p, v) __builtin_amdgcn_raw_buffer_store_b128(v, rs, (int)((const char*)(p) - (const char*)(b0)), 0, 16)
; __device__ __forceinline__ unsigned cvt_pk_bf16(float lo, float hi) { unsigned r; asm volatile("v_cvt_pk_bf16_f32 %0, %1, %2" : "=v"(r) : "v"(lo), "v"(hi)); return r; }
;     __device__ __forceinline__ void operator()(const f32x4 (&acc)[2][2][4][2], const Unit& u, int wr, int wc, int fr, int fq) const {
;     ...
;             for (int m = 0; m < 4; ++m) { const size_t off = (size_t)(row0 + ai * HALF + m * 16) * ldc + col0;
; #pragma unroll
;                 for (int bj = 0; bj < 2; ++bj) {
;                     if (BASE_F32) { b0[m][bj] = *(const f32x4*)((const float*)base + off + bj * HALF); b1[m][bj] = *(const f32x4*)((const float*)base + off + bj * HALF + 4); }
;                     else { const u32x4 q = *(const u32x4*)((const bf16_t*)base + off + bj * HALF);
;                         b0[m][bj] = (f32x4){__uint_as_float(q.x << 16), __uint_as_float(q.x & 0xffff0000u), __uint_as_float(q.y << 16), __uint_as_float(q.y & 0xffff0000u)};
;                         b1[m][bj] = (f32x4){__uint_as_float(q.z << 16), __uint_as_float(q.z & 0xffff0000u), __uint_as_float(q.w << 16), __uint_as_float(q.w & 0xffff0000u)}; } } }
;             asm volatile("" ::: "memory");
; #pragma unroll
;             for (int m = 0; m < 4; ++m) { const size_t off = (size_t)(row0 + ai * HALF + m * 16) * ldc + col0; float ssq = 0.f;
; #pragma unroll
;                 for (int bj = 0; bj < 2; ++bj) {
;                     const f32x4 o0 = b0[m][bj] + acc[ai][bj][m][0] * sc, o1 = b1[m][bj] + acc[ai][bj][m][1] * sc;
;                     ssq += ((o0[0] * o0[0] + o0[1] * o0[1]) + (o0[2] * o0[2] + o0[3] * o0[3])) + ((o1[0] * o1[0] + o1[1] * o1[1]) + (o1[2] * o1[2] + o1[3] * o1[3]));
;                     u32x4 w; w.x = cvt_pk_bf16(o0[0], o0[1]); w.y = cvt_pk_bf16(o0[2], o0[3]); w.z = cvt_pk_bf16(o1[0], o1[1]); w.w = cvt_pk_bf16(o1[2], o1[3]);
;                     PG8_ST16(rs_, out, out + off + bj * HALF, w); }
;                 ssq += __shfl_xor(ssq, 16); ssq += __shfl_xor(ssq, 32);
;                 if (fq == 0) rowss[(size_t)(row0 + ai * HALF + m * 16) * 32 + 4 * u.pn + wc] = ssq; }
.LBB0_871:
	v_lshrrev_b32_e32 v252, 2, v215
	v_and_b32_e32 v207, 15, v215
	v_sub_u32_e32 v252, v252, v207
	v_lshlrev_b32_e32 v207, 4, v207
	v_lshrrev_b32_e32 v249, 4, v215
	v_lshl_or_b32 v249, v249, 2, v207
	v_and_b32_e32 v207, 3, v215
	v_lshrrev_b32_e32 v248, 4, v215
	v_sub_u32_e32 v248, v207, v248
	v_lshlrev_b32_e32 v238, 12, v252
	v_lshl_add_u32 v238, v248, 4, v238
	v_ashrrev_i32_e32 v239, 31, v238
	v_lshlrev_b32_e32 v240, 1, v238
	v_ashrrev_i32_e32 v241, 31, v240
	v_and_b32_e32 v248, 60, v215
	v_lshl_or_b32 v248, v207, 6, v248
	v_lshl_add_u32 v194, s69, 8, v208
	v_lshl_or_b32 v190, s68, 8, v218
	v_ashrrev_i32_e32 v191, 31, v190
	v_ashrrev_i32_e32 v195, 31, v194
	v_lshl_add_u64 v[192:193], v[190:191], 2, s[18:19]
	v_lshl_add_u64 v[192:193], v[192:193], 0, v[240:241]
	v_lshlrev_b64 v[132:133], 13, v[194:195]
	v_lshl_add_u64 v[132:133], v[192:193], 0, v[132:133]
	global_load_dwordx4 v[198:201], v[132:133], off offset:16
	global_load_dwordx4 v[220:223], v[132:133], off
	global_load_dwordx4 v[224:227], v[132:133], off offset:528
	global_load_dwordx4 v[228:231], v[132:133], off offset:512
	v_or_b32_e32 v204, 16, v194
	v_ashrrev_i32_e32 v205, 31, v204
	v_lshlrev_b64 v[132:133], 13, v[204:205]
	v_or_b32_e32 v202, 32, v194
	v_lshl_add_u64 v[132:133], v[192:193], 0, v[132:133]
	v_ashrrev_i32_e32 v203, 31, v202
	global_load_dwordx4 v[172:175], v[132:133], off offset:16
	global_load_dwordx4 v[176:179], v[132:133], off
	global_load_dwordx4 v[164:167], v[132:133], off offset:528
	global_load_dwordx4 v[168:171], v[132:133], off offset:512
	v_lshlrev_b64 v[132:133], 13, v[202:203]
	v_or_b32_e32 v196, 48, v194
	v_lshl_add_u64 v[132:133], v[192:193], 0, v[132:133]
	v_ashrrev_i32_e32 v197, 31, v196
	global_load_dwordx4 v[156:159], v[132:133], off offset:16
	global_load_dwordx4 v[160:163], v[132:133], off
	global_load_dwordx4 v[140:143], v[132:133], off offset:528
	global_load_dwordx4 v[148:151], v[132:133], off offset:512
	v_lshlrev_b64 v[132:133], 13, v[196:197]
	v_lshl_add_u64 v[136:137], v[192:193], 0, v[132:133]
	global_load_dwordx4 v[144:147], v[136:137], off offset:16
	global_load_dwordx4 v[152:155], v[136:137], off
	global_load_dwordx4 v[132:135], v[136:137], off offset:528
	s_nop 0
	global_load_dwordx4 v[136:139], v[136:137], off offset:512
	s_lshl_b32 s42, s68, 2
	s_ashr_i32 s43, s42, 31
	s_waitcnt vmcnt(0)
	ds_bpermute_b32 v198, v249, v198
	ds_bpermute_b32 v199, v249, v199
	ds_bpermute_b32 v200, v249, v200
	ds_bpermute_b32 v201, v249, v201
	ds_bpermute_b32 v220, v249, v220
	ds_bpermute_b32 v221, v249, v221
	ds_bpermute_b32 v222, v249, v222
	ds_bpermute_b32 v223, v249, v223
	ds_bpermute_b32 v224, v249, v224
	ds_bpermute_b32 v225, v249, v225
	ds_bpermute_b32 v226, v249, v226
	ds_bpermute_b32 v227, v249, v227
	ds_bpermute_b32 v228, v249, v228
	ds_bpermute_b32 v229, v249, v229
	ds_bpermute_b32 v230, v249, v230
	ds_bpermute_b32 v231, v249, v231
	ds_bpermute_b32 v172, v249, v172
	ds_bpermute_b32 v173, v249, v173
	ds_bpermute_b32 v174, v249, v174
	ds_bpermute_b32 v175, v249, v175
	ds_bpermute_b32 v176, v249, v176
	ds_bpermute_b32 v177, v249, v177
	ds_bpermute_b32 v178, v249, v178
	ds_bpermute_b32 v179, v249, v179
	ds_bpermute_b32 v164, v249, v164
	ds_bpermute_b32 v165, v249, v165
	ds_bpermute_b32 v166, v249, v166
	ds_bpermute_b32 v167, v249, v167
	ds_bpermute_b32 v168, v249, v168
	ds_bpermute_b32 v169, v249, v169
	ds_bpermute_b32 v170, v249, v170
	ds_bpermute_b32 v171, v249, v171
	ds_bpermute_b32 v156, v249, v156
	ds_bpermute_b32 v157, v249, v157
	ds_bpermute_b32 v158, v249, v158
	ds_bpermute_b32 v159, v249, v159
	ds_bpermute_b32 v160, v249, v160
	ds_bpermute_b32 v161, v249, v161
	ds_bpermute_b32 v162, v249, v162
	ds_bpermute_b32 v163, v249, v163
	ds_bpermute_b32 v140, v249, v140
	ds_bpermute_b32 v141, v249, v141
	ds_bpermute_b32 v142, v249, v142
	ds_bpermute_b32 v143, v249, v143
	ds_bpermute_b32 v148, v249, v148
	ds_bpermute_b32 v149, v249, v149
	ds_bpermute_b32 v150, v249, v150
	ds_bpermute_b32 v151, v249, v151
	ds_bpermute_b32 v144, v249, v144
	ds_bpermute_b32 v145, v249, v145
	ds_bpermute_b32 v146, v249, v146
	ds_bpermute_b32 v147, v249, v147
	ds_bpermute_b32 v152, v249, v152
	ds_bpermute_b32 v153, v249, v153
	ds_bpermute_b32 v154, v249, v154
	ds_bpermute_b32 v155, v249, v155
	ds_bpermute_b32 v132, v249, v132
	ds_bpermute_b32 v133, v249, v133
	ds_bpermute_b32 v134, v249, v134
	ds_bpermute_b32 v135, v249, v135
	ds_bpermute_b32 v136, v249, v136
	ds_bpermute_b32 v137, v249, v137
	ds_bpermute_b32 v138, v249, v138
	ds_bpermute_b32 v139, v249, v139
	s_waitcnt lgkmcnt(0)
	v_pk_add_f32 v[128:129], v[128:129], v[198:199]
	v_pk_add_f32 v[126:127], v[126:127], v[222:223]
	v_pk_add_f32 v[124:125], v[124:125], v[220:221]
	v_mul_f32_e32 v199, v127, v127
	v_mul_f32_e32 v198, v125, v125
	v_fmac_f32_e32 v198, v124, v124
	v_fmac_f32_e32 v199, v126, v126
	v_add_f32_e32 v198, v198, v199
	v_mul_f32_e32 v199, v129, v129
	v_fmac_f32_e32 v199, v128, v128
	v_cvt_pk_bf16_f32 v124, v124, v125
	v_cvt_pk_bf16_f32 v125, v126, v127
	v_cvt_pk_bf16_f32 v126, v128, v129
	v_lshlrev_b64 v[128:129], 12, v[194:195]
	v_lshl_add_u64 v[128:129], s[20:21], 0, v[128:129]
	v_lshl_add_u64 v[128:129], v[190:191], 1, v[128:129]
	v_pk_add_f32 v[122:123], v[122:123], v[230:231]
	v_pk_add_f32 v[120:121], v[120:121], v[228:229]
	v_pk_add_f32 v[130:131], v[130:131], v[200:201]
	s_nop 0
	v_cvt_pk_bf16_f32 v127, v130, v131
	v_lshl_add_u64 v[234:235], v[128:129], 0, v[238:239]
	ds_bpermute_b32 v240, v248, v124
	ds_bpermute_b32 v241, v248, v125
	ds_bpermute_b32 v242, v248, v126
	ds_bpermute_b32 v243, v248, v127
	v_mul_f32_e32 v200, v131, v131
	v_fmac_f32_e32 v200, v130, v130
	v_pk_add_f32 v[124:125], v[118:119], v[226:227]
	v_pk_add_f32 v[118:119], v[116:117], v[224:225]
	v_mul_f32_e32 v116, v121, v121
	v_mul_f32_e32 v117, v123, v123
	v_fmac_f32_e32 v116, v120, v120
	v_fmac_f32_e32 v117, v122, v122
	v_add_f32_e32 v116, v116, v117
	v_mul_f32_e32 v117, v119, v119
	v_mul_f32_e32 v126, v125, v125
	v_fmac_f32_e32 v117, v118, v118
	v_fmac_f32_e32 v126, v124, v124
	v_add_f32_e32 v199, v199, v200
	v_add_f32_e32 v117, v117, v126
	v_add_f32_e32 v198, v198, v199
	v_add_f32_e32 v116, v116, v117
	v_add_f32_e32 v126, v198, v116
	v_cvt_pk_bf16_f32 v116, v120, v121
	v_cvt_pk_bf16_f32 v117, v122, v123
	v_cvt_pk_bf16_f32 v118, v118, v119
	v_cvt_pk_bf16_f32 v119, v124, v125
	ds_bpermute_b32 v244, v248, v116
	ds_bpermute_b32 v245, v248, v117
	ds_bpermute_b32 v246, v248, v118
	ds_bpermute_b32 v247, v248, v119
	s_waitcnt lgkmcnt(4)
; #define PG8_ST16(rs, b0, p, v) __builtin_amdgcn_raw_buffer_store_b128(v, rs, (int)((const char*)(p) - (const char*)(b0)), 0, 16)
; __device__ __forceinline__ unsigned cvt_pk_bf16(float lo, float hi) { unsigned r; asm volatile("v_cvt_pk_bf16_f32 %0, %1, %2" : "=v"(r) : "v"(lo), "v"(hi)); return r; }
;     __device__ __forceinline__ void operator()(const f32x4 (&acc)[2][2][4][2], const Unit& u, int wr, int wc, int fr, int fq) const {
;     ...
;             for (int m = 0; m < 4; ++m) { const size_t off = (size_t)(row0 + ai * HALF + m * 16) * ldc + col0;
; #pragma unroll
;                 for (int bj = 0; bj < 2; ++bj) {
;                     if (BASE_F32) { b0[m][bj] = *(const f32x4*)((const float*)base + off + bj * HALF); b1[m][bj] = *(const f32x4*)((const float*)base + off + bj * HALF + 4); }
;                     else { const u32x4 q = *(const u32x4*)((const bf16_t*)base + off + bj * HALF);
;                         b0[m][bj] = (f32x4){__uint_as_float(q.x << 16), __uint_as_float(q.x & 0xffff0000u), __uint_as_float(q.y << 16), __uint_as_float(q.y & 0xffff0000u)};
;                         b1[m][bj] = (f32x4){__uint_as_float(q.z << 16), __uint_as_float(q.z & 0xffff0000u), __uint_as_float(q.w << 16), __uint_as_float(q.w & 0xffff0000u)}; } } }
;             asm volatile("" ::: "memory");
; #pragma unroll
;             for (int m = 0; m < 4; ++m) { const size_t off = (size_t)(row0 + ai * HALF + m * 16) * ldc + col0; float ssq = 0.f;
; #pragma unroll
;                 for (int bj = 0; bj < 2; ++bj) {
;                     const f32x4 o0 = b0[m][bj] + acc[ai][bj][m][0] * sc, o1 = b1[m][bj] + acc[ai][bj][m][1] * sc;
;                     ssq += ((o0[0] * o0[0] + o0[1] * o0[1]) + (o0[2] * o0[2] + o0[3] * o0[3])) + ((o1[0] * o1[0] + o1[1] * o1[1]) + (o1[2] * o1[2] + o1[3] * o1[3]));
;                     u32x4 w; w.x = cvt_pk_bf16(o0[0], o0[1]); w.y = cvt_pk_bf16(o0[2], o0[3]); w.z = cvt_pk_bf16(o1[0], o1[1]); w.w = cvt_pk_bf16(o1[2], o1[3]);
;                     PG8_ST16(rs_, out, out + off + bj * HALF, w); }
;                 ssq += __shfl_xor(ssq, 16); ssq += __shfl_xor(ssq, 32);
;                 if (fq == 0) rowss[(size_t)(row0 + ai * HALF + m * 16) * 32 + 4 * u.pn + wc] = ssq; }
	global_store_dwordx4 v[234:235], v[240:243], off
	s_nop 1
	v_and_b32_e32 v117, 64, v215
	v_xor_b32_e32 v116, 16, v215
	v_add_u32_e32 v117, 64, v117
	v_cmp_lt_i32_e32 vcc, v116, v117
	v_xor_b32_e32 v118, 32, v215
	s_nop 0
	v_cndmask_b32_e32 v116, v215, v116, vcc
	v_lshlrev_b32_e32 v220, 2, v116
	v_mov_b32_e32 v116, v126
	s_nop 1
	v_permlane16_swap_b32_e32 v116, v126
	v_cmp_lt_i32_e32 vcc, v118, v117
	s_waitcnt lgkmcnt(0)
	v_add_f32_e32 v116, v126, v116
	v_cndmask_b32_e32 v117, v215, v118, vcc
	v_lshlrev_b32_e32 v221, 2, v117
	v_mov_b32_e32 v117, v116
	s_nop 1
	v_permlane32_swap_b32_e32 v117, v116
	s_and_saveexec_b64 s[44:45], s[2:3]
	s_cbranch_execz .LBB0_873
	v_lshlrev_b64 v[118:119], 7, v[194:195]
	v_lshl_add_u64 v[118:119], s[22:23], 0, v[118:119]
	v_lshl_add_u64 v[118:119], s[42:43], 2, v[118:119]
	s_lshl_b32 s68, s60, 2
	s_mov_b32 s69, s31
	v_lshl_add_u64 v[118:119], v[118:119], 0, s[68:69]
	s_waitcnt lgkmcnt(0)
	v_add_f32_e32 v116, v116, v117
	global_store_dword v[118:119], v116, off
.LBB0_873:
	s_or_b64 exec, exec, s[44:45]
	v_pk_add_f32 v[114:115], v[114:115], v[178:179]
	v_pk_add_f32 v[112:113], v[112:113], v[176:177]
	v_pk_add_f32 v[118:119], v[110:111], v[174:175]
	v_pk_add_f32 v[110:111], v[108:109], v[172:173]
	v_mul_f32_e32 v108, v113, v113
	v_mul_f32_e32 v109, v115, v115
	v_fmac_f32_e32 v108, v112, v112
	v_fmac_f32_e32 v109, v114, v114
	v_add_f32_e32 v108, v108, v109
	v_mul_f32_e32 v109, v111, v111
	v_mul_f32_e32 v120, v119, v119
	v_fmac_f32_e32 v109, v110, v110
	v_fmac_f32_e32 v120, v118, v118
	v_add_f32_e32 v109, v109, v120
	v_pk_add_f32 v[106:107], v[106:107], v[170:171]
	v_pk_add_f32 v[104:105], v[104:105], v[168:169]
	v_add_f32_e32 v120, v108, v109
	v_cvt_pk_bf16_f32 v108, v112, v113
	v_cvt_pk_bf16_f32 v109, v114, v115
	v_pk_add_f32 v[114:115], v[100:101], v[164:165]
	v_mul_f32_e32 v100, v105, v105
	v_mul_f32_e32 v101, v107, v107
	v_pk_add_f32 v[112:113], v[102:103], v[166:167]
	v_fmac_f32_e32 v100, v104, v104
	v_fmac_f32_e32 v101, v106, v106
	v_add_f32_e32 v100, v100, v101
	v_mul_f32_e32 v101, v115, v115
	v_mul_f32_e32 v102, v113, v113
	v_fmac_f32_e32 v101, v114, v114
	v_fmac_f32_e32 v102, v112, v112
	v_add_f32_e32 v101, v101, v102
	v_add_f32_e32 v100, v100, v101
	v_add_f32_e32 v103, v120, v100
	v_cvt_pk_bf16_f32 v110, v110, v111
	v_cvt_pk_bf16_f32 v111, v118, v119
	v_mov_b32_e32 v118, v103
	s_nop 1
	v_permlane16_swap_b32_e32 v118, v103
	s_waitcnt lgkmcnt(1)
	v_lshlrev_b64 v[116:117], 11, v[204:205]
	v_lshl_add_u64 v[100:101], v[116:117], 1, s[20:21]
	v_lshl_add_u64 v[116:117], v[190:191], 1, v[100:101]
	v_lshl_add_u64 v[236:237], v[116:117], 0, v[238:239]
	ds_bpermute_b32 v240, v248, v108
	ds_bpermute_b32 v241, v248, v109
	ds_bpermute_b32 v242, v248, v110
	ds_bpermute_b32 v243, v248, v111
	s_waitcnt lgkmcnt(4)
	global_store_dwordx4 v[234:235], v[244:247], off offset:256
	s_waitcnt lgkmcnt(0)
	v_add_f32_e32 v100, v103, v118
	v_mov_b32_e32 v101, v100
	s_nop 1
	v_permlane32_swap_b32_e32 v101, v100
	v_cvt_pk_bf16_f32 v102, v104, v105
	v_cvt_pk_bf16_f32 v103, v106, v107
	v_cvt_pk_bf16_f32 v104, v114, v115
	v_cvt_pk_bf16_f32 v105, v112, v113
	ds_bpermute_b32 v244, v248, v102
	ds_bpermute_b32 v245, v248, v103
	ds_bpermute_b32 v246, v248, v104
	ds_bpermute_b32 v247, v248, v105
	s_waitcnt lgkmcnt(4)
	global_store_dwordx4 v[236:237], v[240:243], off
	s_and_saveexec_b64 s[44:45], s[2:3]
	s_cbranch_execz .LBB0_875
	v_lshlrev_b64 v[102:103], 7, v[204:205]
	v_lshl_add_u64 v[102:103], s[22:23], 0, v[102:103]
	v_lshl_add_u64 v[102:103], s[42:43], 2, v[102:103]
	s_lshl_b32 s68, s60, 2
	s_mov_b32 s69, s31
	v_lshl_add_u64 v[102:103], v[102:103], 0, s[68:69]
	s_waitcnt lgkmcnt(0)
	v_add_f32_e32 v100, v100, v101
	global_store_dword v[102:103], v100, off
.LBB0_875:
	s_or_b64 exec, exec, s[44:45]
	v_pk_add_f32 v[98:99], v[98:99], v[162:163]
	v_pk_add_f32 v[96:97], v[96:97], v[160:161]
	v_pk_add_f32 v[102:103], v[94:95], v[158:159]
	v_pk_add_f32 v[94:95], v[92:93], v[156:157]
	v_mul_f32_e32 v92, v97, v97
	v_mul_f32_e32 v93, v99, v99
	v_fmac_f32_e32 v92, v96, v96
	v_fmac_f32_e32 v93, v98, v98
	v_add_f32_e32 v92, v92, v93
	v_mul_f32_e32 v93, v95, v95
	v_mul_f32_e32 v104, v103, v103
	v_fmac_f32_e32 v93, v94, v94
	v_fmac_f32_e32 v104, v102, v102
	v_add_f32_e32 v93, v93, v104
	v_pk_add_f32 v[90:91], v[90:91], v[150:151]
	v_pk_add_f32 v[88:89], v[88:89], v[148:149]
	v_add_f32_e32 v104, v92, v93
	v_cvt_pk_bf16_f32 v92, v96, v97
	v_cvt_pk_bf16_f32 v93, v98, v99
	v_pk_add_f32 v[98:99], v[84:85], v[140:141]
	v_mul_f32_e32 v84, v89, v89
	v_mul_f32_e32 v85, v91, v91
	v_pk_add_f32 v[96:97], v[86:87], v[142:143]
	v_fmac_f32_e32 v84, v88, v88
	v_fmac_f32_e32 v85, v90, v90
	v_add_f32_e32 v84, v84, v85
	v_mul_f32_e32 v85, v99, v99
	v_mul_f32_e32 v86, v97, v97
	v_fmac_f32_e32 v85, v98, v98
	v_fmac_f32_e32 v86, v96, v96
	v_add_f32_e32 v85, v85, v86
	v_add_f32_e32 v84, v84, v85
	v_add_f32_e32 v87, v104, v84
	v_cvt_pk_bf16_f32 v94, v94, v95
	v_cvt_pk_bf16_f32 v95, v102, v103
	v_mov_b32_e32 v102, v87
	s_nop 1
	v_permlane16_swap_b32_e32 v102, v87
	s_waitcnt lgkmcnt(1)
	v_lshlrev_b64 v[100:101], 11, v[202:203]
	v_lshl_add_u64 v[84:85], v[100:101], 1, s[20:21]
	v_lshl_add_u64 v[100:101], v[190:191], 1, v[84:85]
	v_lshl_add_u64 v[234:235], v[100:101], 0, v[238:239]
	ds_bpermute_b32 v240, v248, v92
	ds_bpermute_b32 v241, v248, v93
	ds_bpermute_b32 v242, v248, v94
	ds_bpermute_b32 v243, v248, v95
	s_waitcnt lgkmcnt(4)
	global_store_dwordx4 v[236:237], v[244:247], off offset:256
	s_waitcnt lgkmcnt(0)
	v_add_f32_e32 v84, v87, v102
	v_mov_b32_e32 v85, v84
	s_nop 1
	v_permlane32_swap_b32_e32 v85, v84
	v_cvt_pk_bf16_f32 v86, v88, v89
	v_cvt_pk_bf16_f32 v87, v90, v91
	v_cvt_pk_bf16_f32 v88, v98, v99
	v_cvt_pk_bf16_f32 v89, v96, v97
	ds_bpermute_b32 v244, v248, v86
	ds_bpermute_b32 v245, v248, v87
	ds_bpermute_b32 v246, v248, v88
	ds_bpermute_b32 v247, v248, v89
	s_waitcnt lgkmcnt(4)
	global_store_dwordx4 v[234:235], v[240:243], off
	s_and_saveexec_b64 s[44:45], s[2:3]
	s_cbranch_execz .LBB0_877
	v_lshlrev_b64 v[86:87], 7, v[202:203]
	v_lshl_add_u64 v[86:87], s[22:23], 0, v[86:87]
	v_lshl_add_u64 v[86:87], s[42:43], 2, v[86:87]
	s_lshl_b32 s68, s60, 2
	s_mov_b32 s69, s31
	v_lshl_add_u64 v[86:87], v[86:87], 0, s[68:69]
	s_waitcnt lgkmcnt(0)
	v_add_f32_e32 v84, v84, v85
	global_store_dword v[86:87], v84, off
; #define PG8_ST16(rs, b0, p, v) __builtin_amdgcn_raw_buffer_store_b128(v, rs, (int)((const char*)(p) - (const char*)(b0)), 0, 16)
; __device__ __forceinline__ unsigned cvt_pk_bf16(float lo, float hi) { unsigned r; asm volatile("v_cvt_pk_bf16_f32 %0, %1, %2" : "=v"(r) : "v"(lo), "v"(hi)); return r; }
;     __device__ __forceinline__ void operator()(const f32x4 (&acc)[2][2][4][2], const Unit& u, int wr, int wc, int fr, int fq) const {
;     ...
;             for (int m = 0; m < 4; ++m) { const size_t off = (size_t)(row0 + ai * HALF + m * 16) * ldc + col0;
; #pragma unroll
;                 for (int bj = 0; bj < 2; ++bj) {
;                     if (BASE_F32) { b0[m][bj] = *(const f32x4*)((const float*)base + off + bj * HALF); b1[m][bj] = *(const f32x4*)((const float*)base + off + bj * HALF + 4); }
;                     else { const u32x4 q = *(const u32x4*)((const bf16_t*)base + off + bj * HALF);
;                         b0[m][bj] = (f32x4){__uint_as_float(q.x << 16), __uint_as_float(q.x & 0xffff0000u), __uint_as_float(q.y << 16), __uint_as_float(q.y & 0xffff0000u)};
;                         b1[m][bj] = (f32x4){__uint_as_float(q.z << 16), __uint_as_float(q.z & 0xffff0000u), __uint_as_float(q.w << 16), __uint_as_float(q.w & 0xffff0000u)}; } } }
;             asm volatile("" ::: "memory");
; #pragma unroll
;             for (int m = 0; m < 4; ++m) { const size_t off = (size_t)(row0 + ai * HALF + m * 16) * ldc + col0; float ssq = 0.f;
; #pragma unroll
;                 for (int bj = 0; bj < 2; ++bj) {
;                     const f32x4 o0 = b0[m][bj] + acc[ai][bj][m][0] * sc, o1 = b1[m][bj] + acc[ai][bj][m][1] * sc;
;                     ssq += ((o0[0] * o0[0] + o0[1] * o0[1]) + (o0[2] * o0[2] + o0[3] * o0[3])) + ((o1[0] * o1[0] + o1[1] * o1[1]) + (o1[2] * o1[2] + o1[3] * o1[3]));
;                     u32x4 w; w.x = cvt_pk_bf16(o0[0], o0[1]); w.y = cvt_pk_bf16(o0[2], o0[3]); w.z = cvt_pk_bf16(o1[0], o1[1]); w.w = cvt_pk_bf16(o1[2], o1[3]);
;                     PG8_ST16(rs_, out, out + off + bj * HALF, w); }
;                 ssq += __shfl_xor(ssq, 16); ssq += __shfl_xor(ssq, 32);
;                 if (fq == 0) rowss[(size_t)(row0 + ai * HALF + m * 16) * 32 + 4 * u.pn + wc] = ssq; }
.LBB0_877:
	s_or_b64 exec, exec, s[44:45]
	v_pk_add_f32 v[82:83], v[82:83], v[154:155]
	v_pk_add_f32 v[80:81], v[80:81], v[152:153]
	v_pk_add_f32 v[86:87], v[78:79], v[146:147]
	v_pk_add_f32 v[78:79], v[76:77], v[144:145]
	v_mul_f32_e32 v76, v81, v81
	v_mul_f32_e32 v77, v83, v83
	v_fmac_f32_e32 v76, v80, v80
	v_fmac_f32_e32 v77, v82, v82
	v_add_f32_e32 v76, v76, v77
	v_mul_f32_e32 v77, v79, v79
	v_mul_f32_e32 v88, v87, v87
	v_fmac_f32_e32 v77, v78, v78
	v_fmac_f32_e32 v88, v86, v86
	v_add_f32_e32 v77, v77, v88
	v_pk_add_f32 v[74:75], v[74:75], v[138:139]
	v_pk_add_f32 v[72:73], v[72:73], v[136:137]
	v_add_f32_e32 v88, v76, v77
	v_cvt_pk_bf16_f32 v76, v80, v81
	v_cvt_pk_bf16_f32 v77, v82, v83
	v_pk_add_f32 v[82:83], v[68:69], v[132:133]
	v_mul_f32_e32 v68, v73, v73
	v_mul_f32_e32 v69, v75, v75
	v_pk_add_f32 v[80:81], v[70:71], v[134:135]
	v_fmac_f32_e32 v68, v72, v72
	v_fmac_f32_e32 v69, v74, v74
	v_add_f32_e32 v68, v68, v69
	v_mul_f32_e32 v69, v83, v83
	v_mul_f32_e32 v70, v81, v81
	v_fmac_f32_e32 v69, v82, v82
	v_fmac_f32_e32 v70, v80, v80
	v_add_f32_e32 v69, v69, v70
	v_add_f32_e32 v68, v68, v69
	v_add_f32_e32 v71, v88, v68
	v_cvt_pk_bf16_f32 v78, v78, v79
	v_cvt_pk_bf16_f32 v79, v86, v87
	v_mov_b32_e32 v86, v71
	s_nop 1
	v_permlane16_swap_b32_e32 v86, v71
	s_waitcnt lgkmcnt(1)
	v_lshlrev_b64 v[84:85], 11, v[196:197]
	v_lshl_add_u64 v[68:69], v[84:85], 1, s[20:21]
	v_lshl_add_u64 v[84:85], v[190:191], 1, v[68:69]
	v_lshl_add_u64 v[236:237], v[84:85], 0, v[238:239]
	ds_bpermute_b32 v240, v248, v76
	ds_bpermute_b32 v241, v248, v77
	ds_bpermute_b32 v242, v248, v78
	ds_bpermute_b32 v243, v248, v79
	s_waitcnt lgkmcnt(4)
	global_store_dwordx4 v[234:235], v[244:247], off offset:256
	s_waitcnt lgkmcnt(0)
	v_add_f32_e32 v68, v71, v86
	v_mov_b32_e32 v69, v68
	s_nop 1
	v_permlane32_swap_b32_e32 v69, v68
	v_cvt_pk_bf16_f32 v70, v72, v73
	v_cvt_pk_bf16_f32 v71, v74, v75
	v_cvt_pk_bf16_f32 v72, v82, v83
	v_cvt_pk_bf16_f32 v73, v80, v81
	ds_bpermute_b32 v244, v248, v70
	ds_bpermute_b32 v245, v248, v71
	ds_bpermute_b32 v246, v248, v72
	ds_bpermute_b32 v247, v248, v73
	s_waitcnt lgkmcnt(4)
	global_store_dwordx4 v[236:237], v[240:243], off
	s_waitcnt lgkmcnt(0)
	global_store_dwordx4 v[236:237], v[244:247], off offset:256
	s_and_saveexec_b64 s[44:45], s[2:3]
	s_cbranch_execz .LBB0_879
	v_lshlrev_b64 v[70:71], 7, v[196:197]
	v_lshl_add_u64 v[70:71], s[22:23], 0, v[70:71]
	v_lshl_add_u64 v[70:71], s[42:43], 2, v[70:71]
	s_lshl_b32 s68, s60, 2
	s_mov_b32 s69, s31
	v_lshl_add_u64 v[70:71], v[70:71], 0, s[68:69]
	s_waitcnt lgkmcnt(0)
	v_add_f32_e32 v68, v68, v69
	global_store_dword v[70:71], v68, off
.LBB0_879:
	s_or_b64 exec, exec, s[44:45]
	v_add_u32_e32 v130, 0x80, v194
	v_ashrrev_i32_e32 v131, 31, v130
	s_waitcnt lgkmcnt(0)
	v_lshlrev_b64 v[68:69], 13, v[130:131]
	v_lshl_add_u64 v[68:69], v[192:193], 0, v[68:69]
	global_load_dwordx4 v[132:135], v[68:69], off offset:16
	global_load_dwordx4 v[136:139], v[68:69], off
	global_load_dwordx4 v[116:119], v[68:69], off offset:528
	global_load_dwordx4 v[120:123], v[68:69], off offset:512
	v_add_u32_e32 v128, 0x90, v194
	v_ashrrev_i32_e32 v129, 31, v128
	v_lshlrev_b64 v[68:69], 13, v[128:129]
	v_add_u32_e32 v126, 0xa0, v194
	v_lshl_add_u64 v[68:69], v[192:193], 0, v[68:69]
	v_ashrrev_i32_e32 v127, 31, v126
	global_load_dwordx4 v[108:111], v[68:69], off offset:16
	global_load_dwordx4 v[112:115], v[68:69], off
	global_load_dwordx4 v[100:103], v[68:69], off offset:528
	global_load_dwordx4 v[104:107], v[68:69], off offset:512
	v_lshlrev_b64 v[68:69], 13, v[126:127]
	v_add_u32_e32 v124, 0xb0, v194
	v_lshl_add_u64 v[68:69], v[192:193], 0, v[68:69]
	v_ashrrev_i32_e32 v125, 31, v124
	global_load_dwordx4 v[92:95], v[68:69], off offset:16
	global_load_dwordx4 v[96:99], v[68:69], off
	global_load_dwordx4 v[76:79], v[68:69], off offset:528
	global_load_dwordx4 v[84:87], v[68:69], off offset:512
	v_lshlrev_b64 v[68:69], 13, v[124:125]
	v_lshl_add_u64 v[72:73], v[192:193], 0, v[68:69]
	global_load_dwordx4 v[80:83], v[72:73], off offset:16
	global_load_dwordx4 v[88:91], v[72:73], off
	global_load_dwordx4 v[68:71], v[72:73], off offset:528
	s_nop 0
	global_load_dwordx4 v[72:75], v[72:73], off offset:512
	s_waitcnt vmcnt(0)
	ds_bpermute_b32 v132, v249, v132
	ds_bpermute_b32 v133, v249, v133
	ds_bpermute_b32 v134, v249, v134
	ds_bpermute_b32 v135, v249, v135
	ds_bpermute_b32 v136, v249, v136
	ds_bpermute_b32 v137, v249, v137
	ds_bpermute_b32 v138, v249, v138
	ds_bpermute_b32 v139, v249, v139
	ds_bpermute_b32 v116, v249, v116
	ds_bpermute_b32 v117, v249, v117
	ds_bpermute_b32 v118, v249, v118
	ds_bpermute_b32 v119, v249, v119
	ds_bpermute_b32 v120, v249, v120
	ds_bpermute_b32 v121, v249, v121
	ds_bpermute_b32 v122, v249, v122
	ds_bpermute_b32 v123, v249, v123
	ds_bpermute_b32 v108, v249, v108
	ds_bpermute_b32 v109, v249, v109
	ds_bpermute_b32 v110, v249, v110
	ds_bpermute_b32 v111, v249, v111
	ds_bpermute_b32 v112, v249, v112
	ds_bpermute_b32 v113, v249, v113
	ds_bpermute_b32 v114, v249, v114
	ds_bpermute_b32 v115, v249, v115
	ds_bpermute_b32 v100, v249, v100
	ds_bpermute_b32 v101, v249, v101
	ds_bpermute_b32 v102, v249, v102
	ds_bpermute_b32 v103, v249, v103
	ds_bpermute_b32 v104, v249, v104
	ds_bpermute_b32 v105, v249, v105
	ds_bpermute_b32 v106, v249, v106
	ds_bpermute_b32 v107, v249, v107
	ds_bpermute_b32 v92, v249, v92
	ds_bpermute_b32 v93, v249, v93
	ds_bpermute_b32 v94, v249, v94
	ds_bpermute_b32 v95, v249, v95
	ds_bpermute_b32 v96, v249, v96
	ds_bpermute_b32 v97, v249, v97
	ds_bpermute_b32 v98, v249, v98
	ds_bpermute_b32 v99, v249, v99
	ds_bpermute_b32 v76, v249, v76
	ds_bpermute_b32 v77, v249, v77
	ds_bpermute_b32 v78, v249, v78
	ds_bpermute_b32 v79, v249, v79
	ds_bpermute_b32 v84, v249, v84
	ds_bpermute_b32 v85, v249, v85
	ds_bpermute_b32 v86, v249, v86
	ds_bpermute_b32 v87, v249, v87
	ds_bpermute_b32 v80, v249, v80
	ds_bpermute_b32 v81, v249, v81
	ds_bpermute_b32 v82, v249, v82
	ds_bpermute_b32 v83, v249, v83
	ds_bpermute_b32 v88, v249, v88
	ds_bpermute_b32 v89, v249, v89
	ds_bpermute_b32 v90, v249, v90
	ds_bpermute_b32 v91, v249, v91
	ds_bpermute_b32 v68, v249, v68
	ds_bpermute_b32 v69, v249, v69
	ds_bpermute_b32 v70, v249, v70
	ds_bpermute_b32 v71, v249, v71
	ds_bpermute_b32 v72, v249, v72
	ds_bpermute_b32 v73, v249, v73
	ds_bpermute_b32 v74, v249, v74
	ds_bpermute_b32 v75, v249, v75
	s_waitcnt lgkmcnt(0)
; #define PG8_ST16(rs, b0, p, v) __builtin_amdgcn_raw_buffer_store_b128(v, rs, (int)((const char*)(p) - (const char*)(b0)), 0, 16)
; __device__ __forceinline__ unsigned cvt_pk_bf16(float lo, float hi) { unsigned r; asm volatile("v_cvt_pk_bf16_f32 %0, %1, %2" : "=v"(r) : "v"(lo), "v"(hi)); return r; }
;     __device__ __forceinline__ void operator()(const f32x4 (&acc)[2][2][4][2], const Unit& u, int wr, int wc, int fr, int fq) const {
;     ...
;             for (int m = 0; m < 4; ++m) { const size_t off = (size_t)(row0 + ai * HALF + m * 16) * ldc + col0;
; #pragma unroll
;                 for (int bj = 0; bj < 2; ++bj) {
;                     if (BASE_F32) { b0[m][bj] = *(const f32x4*)((const float*)base + off + bj * HALF); b1[m][bj] = *(const f32x4*)((const float*)base + off + bj * HALF + 4); }
;                     else { const u32x4 q = *(const u32x4*)((const bf16_t*)base + off + bj * HALF);
;                         b0[m][bj] = (f32x4){__uint_as_float(q.x << 16), __uint_as_float(q.x & 0xffff0000u), __uint_as_float(q.y << 16), __uint_as_float(q.y & 0xffff0000u)};
;                         b1[m][bj] = (f32x4){__uint_as_float(q.z << 16), __uint_as_float(q.z & 0xffff0000u), __uint_as_float(q.w << 16), __uint_as_float(q.w & 0xffff0000u)}; } } }
;             asm volatile("" ::: "memory");
; #pragma unroll
;             for (int m = 0; m < 4; ++m) { const size_t off = (size_t)(row0 + ai * HALF + m * 16) * ldc + col0; float ssq = 0.f;
; #pragma unroll
;                 for (int bj = 0; bj < 2; ++bj) {
;                     const f32x4 o0 = b0[m][bj] + acc[ai][bj][m][0] * sc, o1 = b1[m][bj] + acc[ai][bj][m][1] * sc;
;                     ssq += ((o0[0] * o0[0] + o0[1] * o0[1]) + (o0[2] * o0[2] + o0[3] * o0[3])) + ((o1[0] * o1[0] + o1[1] * o1[1]) + (o1[2] * o1[2] + o1[3] * o1[3]));
;                     u32x4 w; w.x = cvt_pk_bf16(o0[0], o0[1]); w.y = cvt_pk_bf16(o0[2], o0[3]); w.z = cvt_pk_bf16(o1[0], o1[1]); w.w = cvt_pk_bf16(o1[2], o1[3]);
;                     PG8_ST16(rs_, out, out + off + bj * HALF, w); }
;                 ssq += __shfl_xor(ssq, 16); ssq += __shfl_xor(ssq, 32);
;                 if (fq == 0) rowss[(size_t)(row0 + ai * HALF + m * 16) * 32 + 4 * u.pn + wc] = ssq; }
	v_pk_add_f32 v[134:135], v[62:63], v[134:135]
	s_waitcnt vmcnt(14)
	v_pk_add_f32 v[66:67], v[66:67], v[138:139]
	v_pk_add_f32 v[64:65], v[64:65], v[136:137]
	v_pk_add_f32 v[62:63], v[60:61], v[132:133]
	v_mul_f32_e32 v60, v65, v65
	v_mul_f32_e32 v61, v67, v67
	v_fmac_f32_e32 v60, v64, v64
	v_fmac_f32_e32 v61, v66, v66
	v_add_f32_e32 v60, v60, v61
	v_mul_f32_e32 v61, v63, v63
	v_mul_f32_e32 v132, v135, v135
	v_fmac_f32_e32 v61, v62, v62
	v_fmac_f32_e32 v132, v134, v134
	v_add_f32_e32 v61, v61, v132
	v_add_f32_e32 v132, v60, v61
	v_cvt_pk_bf16_f32 v60, v64, v65
	v_lshlrev_b64 v[64:65], 12, v[130:131]
	v_lshl_add_u64 v[64:65], s[20:21], 0, v[64:65]
	v_cvt_pk_bf16_f32 v61, v66, v67
	v_lshl_add_u64 v[64:65], v[190:191], 1, v[64:65]
	s_waitcnt vmcnt(12)
	v_pk_add_f32 v[58:59], v[58:59], v[122:123]
	v_pk_add_f32 v[56:57], v[56:57], v[120:121]
	v_cvt_pk_bf16_f32 v62, v62, v63
	v_cvt_pk_bf16_f32 v63, v134, v135
	v_lshl_add_u64 v[234:235], v[64:65], 0, v[238:239]
	ds_bpermute_b32 v240, v248, v60
	ds_bpermute_b32 v241, v248, v61
	ds_bpermute_b32 v242, v248, v62
	ds_bpermute_b32 v243, v248, v63
	s_nop 1
	v_pk_add_f32 v[60:61], v[54:55], v[118:119]
	v_pk_add_f32 v[54:55], v[52:53], v[116:117]
	v_mul_f32_e32 v52, v57, v57
	v_mul_f32_e32 v53, v59, v59
	v_fmac_f32_e32 v52, v56, v56
	v_fmac_f32_e32 v53, v58, v58
	v_add_f32_e32 v52, v52, v53
	v_mul_f32_e32 v53, v55, v55
	v_mul_f32_e32 v62, v61, v61
	v_fmac_f32_e32 v53, v54, v54
	v_fmac_f32_e32 v62, v60, v60
	v_add_f32_e32 v53, v53, v62
	v_add_f32_e32 v52, v52, v53
	v_add_f32_e32 v62, v132, v52
	v_cvt_pk_bf16_f32 v52, v56, v57
	v_cvt_pk_bf16_f32 v53, v58, v59
	v_cvt_pk_bf16_f32 v54, v54, v55
	v_cvt_pk_bf16_f32 v55, v60, v61
	ds_bpermute_b32 v244, v248, v52
	ds_bpermute_b32 v245, v248, v53
	ds_bpermute_b32 v246, v248, v54
	ds_bpermute_b32 v247, v248, v55
	s_waitcnt lgkmcnt(4)
	global_store_dwordx4 v[234:235], v[240:243], off
	ds_bpermute_b32 v52, v220, v62
	s_waitcnt lgkmcnt(0)
	v_add_f32_e32 v52, v62, v52
	v_mov_b32_e32 v53, v52
	s_nop 1
	v_permlane32_swap_b32_e32 v53, v52
	s_and_saveexec_b64 s[44:45], s[2:3]
	s_cbranch_execz .LBB0_881
	v_lshlrev_b64 v[54:55], 7, v[130:131]
	v_lshl_add_u64 v[54:55], s[22:23], 0, v[54:55]
	v_lshl_add_u64 v[54:55], s[42:43], 2, v[54:55]
	s_lshl_b32 s68, s60, 2
	s_mov_b32 s69, s31
	v_lshl_add_u64 v[54:55], v[54:55], 0, s[68:69]
	s_waitcnt lgkmcnt(0)
	v_add_f32_e32 v52, v52, v53
	global_store_dword v[54:55], v52, off
.LBB0_881:
	s_or_b64 exec, exec, s[44:45]
	s_waitcnt vmcnt(12)
	v_pk_add_f32 v[50:51], v[50:51], v[114:115]
	v_pk_add_f32 v[48:49], v[48:49], v[112:113]
	v_pk_add_f32 v[54:55], v[46:47], v[110:111]
	v_pk_add_f32 v[46:47], v[44:45], v[108:109]
	v_mul_f32_e32 v44, v49, v49
	v_mul_f32_e32 v45, v51, v51
	v_fmac_f32_e32 v44, v48, v48
	v_fmac_f32_e32 v45, v50, v50
	v_add_f32_e32 v44, v44, v45
	v_mul_f32_e32 v45, v47, v47
	v_mul_f32_e32 v56, v55, v55
	v_fmac_f32_e32 v45, v46, v46
	v_fmac_f32_e32 v56, v54, v54
	v_add_f32_e32 v45, v45, v56
	s_waitcnt vmcnt(10)
	v_pk_add_f32 v[42:43], v[42:43], v[106:107]
	v_pk_add_f32 v[40:41], v[40:41], v[104:105]
	v_add_f32_e32 v56, v44, v45
	v_cvt_pk_bf16_f32 v44, v48, v49
	v_cvt_pk_bf16_f32 v45, v50, v51
	v_pk_add_f32 v[50:51], v[36:37], v[100:101]
	v_mul_f32_e32 v36, v41, v41
	v_mul_f32_e32 v37, v43, v43
	v_pk_add_f32 v[48:49], v[38:39], v[102:103]
	v_fmac_f32_e32 v36, v40, v40
	v_fmac_f32_e32 v37, v42, v42
	v_add_f32_e32 v36, v36, v37
	v_mul_f32_e32 v37, v51, v51
	v_mul_f32_e32 v38, v49, v49
	v_fmac_f32_e32 v37, v50, v50
	v_fmac_f32_e32 v38, v48, v48
	v_add_f32_e32 v37, v37, v38
	v_add_f32_e32 v36, v36, v37
	v_add_f32_e32 v39, v56, v36
	v_cvt_pk_bf16_f32 v46, v46, v47
	v_cvt_pk_bf16_f32 v47, v54, v55
	v_mov_b32_e32 v54, v39
	s_nop 1
	v_permlane16_swap_b32_e32 v54, v39
	s_waitcnt lgkmcnt(1)
	v_lshlrev_b64 v[52:53], 11, v[128:129]
	v_lshl_add_u64 v[36:37], v[52:53], 1, s[20:21]
	v_lshl_add_u64 v[52:53], v[190:191], 1, v[36:37]
	v_lshl_add_u64 v[236:237], v[52:53], 0, v[238:239]
	ds_bpermute_b32 v240, v248, v44
	ds_bpermute_b32 v241, v248, v45
	ds_bpermute_b32 v242, v248, v46
	ds_bpermute_b32 v243, v248, v47
	s_waitcnt lgkmcnt(4)
	global_store_dwordx4 v[234:235], v[244:247], off offset:256
	s_waitcnt lgkmcnt(0)
	v_add_f32_e32 v36, v39, v54
	v_mov_b32_e32 v37, v36
	s_nop 1
	v_permlane32_swap_b32_e32 v37, v36
	v_cvt_pk_bf16_f32 v38, v40, v41
	v_cvt_pk_bf16_f32 v39, v42, v43
	v_cvt_pk_bf16_f32 v40, v50, v51
	v_cvt_pk_bf16_f32 v41, v48, v49
	ds_bpermute_b32 v244, v248, v38
	ds_bpermute_b32 v245, v248, v39
	ds_bpermute_b32 v246, v248, v40
	ds_bpermute_b32 v247, v248, v41
	s_waitcnt lgkmcnt(4)
	global_store_dwordx4 v[236:237], v[240:243], off
	s_and_saveexec_b64 s[44:45], s[2:3]
	s_cbranch_execz .LBB0_883
	v_lshlrev_b64 v[38:39], 7, v[128:129]
	v_lshl_add_u64 v[38:39], s[22:23], 0, v[38:39]
	v_lshl_add_u64 v[38:39], s[42:43], 2, v[38:39]
	s_lshl_b32 s68, s60, 2
	s_mov_b32 s69, s31
	v_lshl_add_u64 v[38:39], v[38:39], 0, s[68:69]
	s_waitcnt lgkmcnt(0)
	v_add_f32_e32 v36, v36, v37
	global_store_dword v[38:39], v36, off
; #define PG8_ST16(rs, b0, p, v) __builtin_amdgcn_raw_buffer_store_b128(v, rs, (int)((const char*)(p) - (const char*)(b0)), 0, 16)
; __device__ __forceinline__ unsigned cvt_pk_bf16(float lo, float hi) { unsigned r; asm volatile("v_cvt_pk_bf16_f32 %0, %1, %2" : "=v"(r) : "v"(lo), "v"(hi)); return r; }
;     __device__ __forceinline__ void operator()(const f32x4 (&acc)[2][2][4][2], const Unit& u, int wr, int wc, int fr, int fq) const {
;     ...
;             for (int m = 0; m < 4; ++m) { const size_t off = (size_t)(row0 + ai * HALF + m * 16) * ldc + col0;
; #pragma unroll
;                 for (int bj = 0; bj < 2; ++bj) {
;                     if (BASE_F32) { b0[m][bj] = *(const f32x4*)((const float*)base + off + bj * HALF); b1[m][bj] = *(const f32x4*)((const float*)base + off + bj * HALF + 4); }
;                     else { const u32x4 q = *(const u32x4*)((const bf16_t*)base + off + bj * HALF);
;                         b0[m][bj] = (f32x4){__uint_as_float(q.x << 16), __uint_as_float(q.x & 0xffff0000u), __uint_as_float(q.y << 16), __uint_as_float(q.y & 0xffff0000u)};
;                         b1[m][bj] = (f32x4){__uint_as_float(q.z << 16), __uint_as_float(q.z & 0xffff0000u), __uint_as_float(q.w << 16), __uint_as_float(q.w & 0xffff0000u)}; } } }
;             asm volatile("" ::: "memory");
; #pragma unroll
;             for (int m = 0; m < 4; ++m) { const size_t off = (size_t)(row0 + ai * HALF + m * 16) * ldc + col0; float ssq = 0.f;
; #pragma unroll
;                 for (int bj = 0; bj < 2; ++bj) {
;                     const f32x4 o0 = b0[m][bj] + acc[ai][bj][m][0] * sc, o1 = b1[m][bj] + acc[ai][bj][m][1] * sc;
;                     ssq += ((o0[0] * o0[0] + o0[1] * o0[1]) + (o0[2] * o0[2] + o0[3] * o0[3])) + ((o1[0] * o1[0] + o1[1] * o1[1]) + (o1[2] * o1[2] + o1[3] * o1[3]));
;                     u32x4 w; w.x = cvt_pk_bf16(o0[0], o0[1]); w.y = cvt_pk_bf16(o0[2], o0[3]); w.z = cvt_pk_bf16(o1[0], o1[1]); w.w = cvt_pk_bf16(o1[2], o1[3]);
;                     PG8_ST16(rs_, out, out + off + bj * HALF, w); }
;                 ssq += __shfl_xor(ssq, 16); ssq += __shfl_xor(ssq, 32);
;                 if (fq == 0) rowss[(size_t)(row0 + ai * HALF + m * 16) * 32 + 4 * u.pn + wc] = ssq; }
.LBB0_883:
	s_or_b64 exec, exec, s[44:45]
	s_waitcnt vmcnt(10)
	v_pk_add_f32 v[34:35], v[34:35], v[98:99]
	v_pk_add_f32 v[32:33], v[32:33], v[96:97]
	v_pk_add_f32 v[38:39], v[30:31], v[94:95]
	v_pk_add_f32 v[30:31], v[28:29], v[92:93]
	v_mul_f32_e32 v28, v33, v33
	v_mul_f32_e32 v29, v35, v35
	v_fmac_f32_e32 v28, v32, v32
	v_fmac_f32_e32 v29, v34, v34
	v_add_f32_e32 v28, v28, v29
	v_mul_f32_e32 v29, v31, v31
	v_mul_f32_e32 v40, v39, v39
	v_fmac_f32_e32 v29, v30, v30
	v_fmac_f32_e32 v40, v38, v38
	v_add_f32_e32 v29, v29, v40
	s_waitcnt vmcnt(8)
	v_pk_add_f32 v[26:27], v[26:27], v[86:87]
	v_pk_add_f32 v[24:25], v[24:25], v[84:85]
	v_add_f32_e32 v40, v28, v29
	v_cvt_pk_bf16_f32 v28, v32, v33
	v_cvt_pk_bf16_f32 v29, v34, v35
	v_pk_add_f32 v[34:35], v[20:21], v[76:77]
	v_mul_f32_e32 v20, v25, v25
	v_mul_f32_e32 v21, v27, v27
	v_pk_add_f32 v[32:33], v[22:23], v[78:79]
	v_fmac_f32_e32 v20, v24, v24
	v_fmac_f32_e32 v21, v26, v26
	v_add_f32_e32 v20, v20, v21
	v_mul_f32_e32 v21, v35, v35
	v_mul_f32_e32 v22, v33, v33
	v_fmac_f32_e32 v21, v34, v34
	v_fmac_f32_e32 v22, v32, v32
	v_add_f32_e32 v21, v21, v22
	v_add_f32_e32 v20, v20, v21
	v_add_f32_e32 v23, v40, v20
	v_cvt_pk_bf16_f32 v30, v30, v31
	v_cvt_pk_bf16_f32 v31, v38, v39
	v_mov_b32_e32 v38, v23
	s_nop 1
	v_permlane16_swap_b32_e32 v38, v23
	s_waitcnt lgkmcnt(1)
	v_lshlrev_b64 v[36:37], 11, v[126:127]
	v_lshl_add_u64 v[20:21], v[36:37], 1, s[20:21]
	v_lshl_add_u64 v[36:37], v[190:191], 1, v[20:21]
	v_lshl_add_u64 v[234:235], v[36:37], 0, v[238:239]
	ds_bpermute_b32 v240, v248, v28
	ds_bpermute_b32 v241, v248, v29
	ds_bpermute_b32 v242, v248, v30
	ds_bpermute_b32 v243, v248, v31
	s_waitcnt lgkmcnt(4)
	global_store_dwordx4 v[236:237], v[244:247], off offset:256
	s_waitcnt lgkmcnt(0)
	v_add_f32_e32 v20, v23, v38
	v_mov_b32_e32 v21, v20
	s_nop 1
	v_permlane32_swap_b32_e32 v21, v20
	v_cvt_pk_bf16_f32 v22, v24, v25
	v_cvt_pk_bf16_f32 v23, v26, v27
	v_cvt_pk_bf16_f32 v24, v34, v35
	v_cvt_pk_bf16_f32 v25, v32, v33
	ds_bpermute_b32 v244, v248, v22
	ds_bpermute_b32 v245, v248, v23
	ds_bpermute_b32 v246, v248, v24
	ds_bpermute_b32 v247, v248, v25
	s_waitcnt lgkmcnt(4)
	global_store_dwordx4 v[234:235], v[240:243], off
	s_and_saveexec_b64 s[44:45], s[2:3]
	s_cbranch_execz .LBB0_885
	v_lshlrev_b64 v[22:23], 7, v[126:127]
	v_lshl_add_u64 v[22:23], s[22:23], 0, v[22:23]
	v_lshl_add_u64 v[22:23], s[42:43], 2, v[22:23]
	s_lshl_b32 s68, s60, 2
	s_mov_b32 s69, s31
	v_lshl_add_u64 v[22:23], v[22:23], 0, s[68:69]
	s_waitcnt lgkmcnt(0)
	v_add_f32_e32 v20, v20, v21
	global_store_dword v[22:23], v20, off
.LBB0_885:
	s_or_b64 exec, exec, s[44:45]
	s_waitcnt vmcnt(8)
	v_pk_add_f32 v[18:19], v[18:19], v[90:91]
	v_pk_add_f32 v[16:17], v[16:17], v[88:89]
	v_pk_add_f32 v[22:23], v[14:15], v[82:83]
	v_pk_add_f32 v[14:15], v[12:13], v[80:81]
	v_mul_f32_e32 v12, v17, v17
	v_mul_f32_e32 v13, v19, v19
	v_fmac_f32_e32 v12, v16, v16
	v_fmac_f32_e32 v13, v18, v18
	v_add_f32_e32 v12, v12, v13
	v_mul_f32_e32 v13, v15, v15
	v_mul_f32_e32 v24, v23, v23
	v_fmac_f32_e32 v13, v14, v14
	v_fmac_f32_e32 v24, v22, v22
	v_add_f32_e32 v13, v13, v24
	s_waitcnt vmcnt(6)
	v_pk_add_f32 v[10:11], v[10:11], v[74:75]
	v_pk_add_f32 v[8:9], v[8:9], v[72:73]
	v_add_f32_e32 v24, v12, v13
	v_cvt_pk_bf16_f32 v12, v16, v17
	v_cvt_pk_bf16_f32 v13, v18, v19
	v_pk_add_f32 v[18:19], v[4:5], v[68:69]
	v_mul_f32_e32 v4, v9, v9
	v_mul_f32_e32 v5, v11, v11
	v_pk_add_f32 v[16:17], v[6:7], v[70:71]
	v_fmac_f32_e32 v4, v8, v8
	v_fmac_f32_e32 v5, v10, v10
	v_add_f32_e32 v4, v4, v5
	v_mul_f32_e32 v5, v19, v19
	v_mul_f32_e32 v6, v17, v17
	v_fmac_f32_e32 v5, v18, v18
	v_fmac_f32_e32 v6, v16, v16
	v_add_f32_e32 v5, v5, v6
	v_add_f32_e32 v4, v4, v5
	v_add_f32_e32 v7, v24, v4
	v_cvt_pk_bf16_f32 v14, v14, v15
	v_cvt_pk_bf16_f32 v15, v22, v23
	v_mov_b32_e32 v22, v7
	s_nop 1
	v_permlane16_swap_b32_e32 v22, v7
	s_waitcnt lgkmcnt(1)
	v_lshlrev_b64 v[20:21], 11, v[124:125]
	v_lshl_add_u64 v[4:5], v[20:21], 1, s[20:21]
	v_lshl_add_u64 v[20:21], v[190:191], 1, v[4:5]
	v_lshl_add_u64 v[236:237], v[20:21], 0, v[238:239]
	ds_bpermute_b32 v240, v248, v12
	ds_bpermute_b32 v241, v248, v13
	ds_bpermute_b32 v242, v248, v14
	ds_bpermute_b32 v243, v248, v15
	s_waitcnt lgkmcnt(4)
	global_store_dwordx4 v[234:235], v[244:247], off offset:256
	s_waitcnt lgkmcnt(0)
	v_add_f32_e32 v4, v7, v22
	v_mov_b32_e32 v5, v4
	s_nop 1
	v_permlane32_swap_b32_e32 v5, v4
	v_cvt_pk_bf16_f32 v6, v8, v9
	v_cvt_pk_bf16_f32 v7, v10, v11
	v_cvt_pk_bf16_f32 v8, v18, v19
	v_cvt_pk_bf16_f32 v9, v16, v17
	ds_bpermute_b32 v244, v248, v6
	ds_bpermute_b32 v245, v248, v7
	ds_bpermute_b32 v246, v248, v8
	ds_bpermute_b32 v247, v248, v9
	s_waitcnt lgkmcnt(4)
	global_store_dwordx4 v[236:237], v[240:243], off
	s_waitcnt lgkmcnt(0)
	global_store_dwordx4 v[236:237], v[244:247], off offset:256
	s_and_saveexec_b64 s[44:45], s[2:3]
	s_cbranch_execz .LBB0_887
	v_lshlrev_b64 v[6:7], 7, v[124:125]
	v_lshl_add_u64 v[6:7], s[22:23], 0, v[6:7]
	v_lshl_add_u64 v[6:7], s[42:43], 2, v[6:7]
	s_lshl_b32 s42, s60, 2
	s_mov_b32 s43, s31
	v_lshl_add_u64 v[6:7], v[6:7], 0, s[42:43]
	s_waitcnt lgkmcnt(0)
	v_add_f32_e32 v4, v4, v5
	global_store_dword v[6:7], v4, off
